# adds MoBA: accumulators in place on past-block steps, gate loads in flight together; K/V fragment LDS waits split
# speedup vs baseline: 1.0040x; 1.0040x over previous
; template <int MODE>
; __device__ __forceinline__ void attn_fox_sub(const bf16x8 (&qr)[4], f32x16& O0, f32x16& O1, float& m, float& l, unsigned saddr  , unsigned cfaddr  , int j, int kv0, int q, int hi) {
;     bf16x8 kf[4], vf[2][2]; f32x4 c0, c1, c2, c3;
;     asm volatile("ds_read_b128 %0, %12\n\tds_read_b128 %1, %12 offset:1024\n\tds_read_b128 %2, %12 offset:2048\n\tds_read_b128 %3, %12 offset:3072\n\t"
;                  "ds_read_b128 %4, %13\n\tds_read_b128 %5, %13 offset:1024\n\tds_read_b128 %6, %13 offset:2048\n\tds_read_b128 %7, %13 offset:3072\n\t"
;                  "ds_read_b128 %8, %14\n\tds_read_b128 %9, %14 offset:16\n\tds_read_b128 %10, %14 offset:64\n\tds_read_b128 %11, %14 offset:80\n\ts_waitcnt lgkmcnt(0)"
;                  : "=&v"(kf[0]), "=&v"(kf[1]), "=&v"(kf[2]), "=&v"(kf[3]), "=&v"(vf[0][0]), "=&v"(vf[0][1]), "=&v"(vf[1][0]), "=&v"(vf[1][1]), "=&v"(c0), "=&v"(c1), "=&v"(c2), "=&v"(c3)
;                  : "v"(saddr + (unsigned)j * 4096u), "v"(saddr + 8192u + (unsigned)j * 4096u), "v"(cfaddr) : "memory");
;     f32x16 S;
;     S[0] = c0[0]; S[1] = c0[1]; S[2] = c0[2]; S[3] = c0[3]; S[4] = c1[0]; S[5] = c1[1]; S[6] = c1[2]; S[7] = c1[3];
;     S[8] = c2[0]; S[9] = c2[1]; S[10] = c2[2]; S[11] = c2[3]; S[12] = c3[0]; S[13] = c3[1]; S[14] = c3[2]; S[15] = c3[3];
; #pragma unroll
;     for (int d0 = 0; d0 < 4; ++d0) S = __builtin_amdgcn_mfma_f32_32x32x16_bf16(kf[d0], qr[d0], S, 0, 0, 0);
;     if (MODE == 1) {
; #pragma unroll
;         for (int r = 0; r < 16; ++r) { const int key = kv0 + (r & 7) + 8 * hi + 16 * (r >> 3); if (key > q) S[r] = -INFINITY; }
;     }
;     float rm = rowmax16_raw(S);
;     { const auto rr = __builtin_amdgcn_permlane32_swap(__float_as_uint(rm), __float_as_uint(rm), false, false); rm = max2_raw(__uint_as_float(rr[0]), __uint_as_float(rr[1])); }
;     if (__any(rm > m)) {
;         const float mn = fmaxf(fmaxf(m, rm), -1e30f); const float alpha = __builtin_amdgcn_exp2f(m - mn);
;         l *= alpha; O0 *= alpha; O1 *= alpha; m = mn; }
;     float p[16]; float ps = 0.f;
; #pragma unroll
;     for (int r = 0; r < 16; ++r) { p[r] = __builtin_amdgcn_exp2f(S[r] - m); ps += p[r]; }
;     l += ps;
;     u32x4 w0, w1;
;     w0.x = pk2(p[0], p[1]); w0.y = pk2(p[2], p[3]); w0.z = pk2(p[4], p[5]); w0.w = pk2(p[6], p[7]);
.LBB0_552:
	s_add_i32 s0, s0, 3
	s_cmp_gt_i32 s0, s14
	s_cbranch_scc1 .LBB0_542
	v_lshl_add_u32 v131, s15, 14, v149
	s_cmp_lg_u32 s16, s91
	s_mov_b64 s[0:1], -1
	s_cbranch_scc0 .LBB0_559
	v_add_u32_e32 v48, 0x80, v153
	v_add_u32_e32 v49, 0x1000, v131
	v_add_u32_e32 v50, 0x3000, v131
	ds_read_b128 v[32:35], v49
	ds_read_b128 v[36:39], v49 offset:1024
	ds_read_b128 v[40:43], v49 offset:2048
	ds_read_b128 v[44:47], v49 offset:3072
	ds_read_b128 v[64:67], v48
	ds_read_b128 v[68:71], v48 offset:16
	ds_read_b128 v[72:75], v48 offset:64
	ds_read_b128 v[76:79], v48 offset:80
	ds_read_b128 v[108:111], v50
	ds_read_b128 v[100:103], v50 offset:1024
	ds_read_b128 v[104:107], v50 offset:2048
	ds_read_b128 v[96:99], v50 offset:3072
	s_waitcnt lgkmcnt(4)
	v_mov_b32_e32 v155, v154
	v_mfma_f32_32x32x16_bf16 v[64:79], v[32:35], v[80:83], v[64:79]
	v_mov_b32_e32 v156, v151
	v_mfma_f32_32x32x16_bf16 v[64:79], v[36:39], v[84:87], v[64:79]
	v_mfma_f32_32x32x16_bf16 v[64:79], v[40:43], v[88:91], v[64:79]
	v_mfma_f32_32x32x16_bf16 v[64:79], v[44:47], v[92:95], v[64:79]
	s_nop 11
	v_max3_f32 v50, v64, v65, v66
	v_max3_f32 v48, v67, v68, v69
	v_max3_f32 v49, v70, v71, v72
	v_max3_f32 v50, v50, v48, v49
	v_max3_f32 v48, v73, v74, v75
	v_max3_f32 v49, v76, v77, v78
	v_max3_f32 v48, v48, v49, v79
	v_max_f32 v50, v50, v48
	v_mov_b32_e32 v48, v50
	s_nop 1
	v_permlane32_swap_b32_e32 v50, v48
	v_max_f32 v157, v50, v48
	v_cmp_gt_f32_e32 vcc, v157, v154
	s_cbranch_vccz .LBB0_556
	v_max3_f32 v155, v154, v157, s94
	v_sub_f32_e32 v32, v154, v155
	v_exp_f32_e32 v32, v32
	s_nop 0
	v_mul_f32_e32 v156, v151, v32
	v_pk_mul_f32 v[14:15], v[14:15], v[32:33] op_sel_hi:[1,0]
	v_pk_mul_f32 v[12:13], v[12:13], v[32:33] op_sel_hi:[1,0]
	v_pk_mul_f32 v[10:11], v[10:11], v[32:33] op_sel_hi:[1,0]
	v_pk_mul_f32 v[8:9], v[8:9], v[32:33] op_sel_hi:[1,0]
	v_pk_mul_f32 v[6:7], v[6:7], v[32:33] op_sel_hi:[1,0]
	v_pk_mul_f32 v[4:5], v[4:5], v[32:33] op_sel_hi:[1,0]
	v_pk_mul_f32 v[2:3], v[2:3], v[32:33] op_sel_hi:[1,0]
	v_pk_mul_f32 v[0:1], v[0:1], v[32:33] op_sel_hi:[1,0]
	v_pk_mul_f32 v[30:31], v[30:31], v[32:33] op_sel_hi:[1,0]
	v_pk_mul_f32 v[28:29], v[28:29], v[32:33] op_sel_hi:[1,0]
	v_pk_mul_f32 v[26:27], v[26:27], v[32:33] op_sel_hi:[1,0]
	v_pk_mul_f32 v[24:25], v[24:25], v[32:33] op_sel_hi:[1,0]
	v_pk_mul_f32 v[22:23], v[22:23], v[32:33] op_sel_hi:[1,0]
	v_pk_mul_f32 v[20:21], v[20:21], v[32:33] op_sel_hi:[1,0]
	v_pk_mul_f32 v[18:19], v[18:19], v[32:33] op_sel_hi:[1,0]
	v_pk_mul_f32 v[16:17], v[16:17], v[32:33] op_sel_hi:[1,0]
.LBB0_556:
	v_sub_f32_e32 v64, v64, v155
	v_exp_f32_e32 v64, v64
	v_sub_f32_e32 v65, v65, v155
	v_exp_f32_e32 v65, v65
	v_sub_f32_e32 v66, v66, v155
	v_exp_f32_e32 v66, v66
	v_sub_f32_e32 v67, v67, v155
	v_exp_f32_e32 v67, v67
	v_sub_f32_e32 v68, v68, v155
	v_add_f32_e32 v157, 0, v64
	v_exp_f32_e32 v68, v68
	v_sub_f32_e32 v69, v69, v155
	v_add_f32_e32 v157, v65, v157
	v_exp_f32_e32 v69, v69
	v_sub_f32_e32 v70, v70, v155
	v_add_f32_e32 v157, v66, v157
	v_exp_f32_e32 v70, v70
	v_sub_f32_e32 v71, v71, v155
	v_add_f32_e32 v157, v67, v157
	v_exp_f32_e32 v71, v71
	v_sub_f32_e32 v72, v72, v155
	v_add_f32_e32 v157, v68, v157
	v_exp_f32_e32 v72, v72
	v_sub_f32_e32 v73, v73, v155
	v_add_f32_e32 v157, v69, v157
	v_exp_f32_e32 v73, v73
	v_sub_f32_e32 v74, v74, v155
	v_add_f32_e32 v157, v70, v157
	v_exp_f32_e32 v74, v74
	v_sub_f32_e32 v75, v75, v155
	v_add_f32_e32 v157, v71, v157
	v_exp_f32_e32 v75, v75
	v_sub_f32_e32 v76, v76, v155
	v_cvt_pk_bf16_f32 v64, v64, v65
	v_cvt_pk_bf16_f32 v65, v66, v67
	v_cvt_pk_bf16_f32 v66, v68, v69
	v_cvt_pk_bf16_f32 v67, v70, v71
	v_add_f32_e32 v157, v72, v157
	v_exp_f32_e32 v76, v76
	v_sub_f32_e32 v77, v77, v155
	s_waitcnt lgkmcnt(0)
	v_mfma_f32_32x32x16_bf16 v[0:15], v[108:111], v[64:67], v[0:15]
	v_add_f32_e32 v157, v73, v157
	v_exp_f32_e32 v77, v77
	v_sub_f32_e32 v78, v78, v155
	v_add_f32_e32 v157, v74, v157
	v_exp_f32_e32 v78, v78
	v_sub_f32_e32 v79, v79, v155
	v_add_f32_e32 v157, v75, v157
	v_mfma_f32_32x32x16_bf16 v[16:31], v[100:103], v[64:67], v[16:31]
	v_exp_f32_e32 v79, v79
	v_add_f32_e32 v157, v76, v157
	v_add_f32_e32 v157, v77, v157
	v_add_f32_e32 v157, v78, v157
	v_add_f32_e32 v157, v79, v157
	v_cvt_pk_bf16_f32 v68, v72, v73
	v_cvt_pk_bf16_f32 v69, v74, v75
	v_cvt_pk_bf16_f32 v70, v76, v77
	v_cvt_pk_bf16_f32 v71, v78, v79
	v_add_f32_e32 v156, v156, v157
	v_add_u32_e32 v157, 0x2000, v131
	v_mfma_f32_32x32x16_bf16 v[0:15], v[104:107], v[68:71], v[0:15]
	v_mfma_f32_32x32x16_bf16 v[16:31], v[96:99], v[68:71], v[16:31]
	ds_read_b128 v[158:161], v131
	ds_read_b128 v[162:165], v131 offset:1024
	ds_read_b128 v[166:169], v131 offset:2048
	ds_read_b128 v[170:173], v131 offset:3072
	ds_read_b128 v[64:67], v153
	ds_read_b128 v[68:71], v153 offset:16
	ds_read_b128 v[72:75], v153 offset:64
	ds_read_b128 v[76:79], v153 offset:80
	ds_read_b128 v[108:111], v157
	ds_read_b128 v[100:103], v157 offset:1024
	ds_read_b128 v[104:107], v157 offset:2048
	ds_read_b128 v[96:99], v157 offset:3072
	s_waitcnt lgkmcnt(4)
	s_nop 0
	v_mfma_f32_32x32x16_bf16 v[64:79], v[158:161], v[80:83], v[64:79]
	v_mfma_f32_32x32x16_bf16 v[64:79], v[162:165], v[84:87], v[64:79]
	v_mfma_f32_32x32x16_bf16 v[64:79], v[166:169], v[88:91], v[64:79]
	v_mfma_f32_32x32x16_bf16 v[64:79], v[170:173], v[92:95], v[64:79]
	s_nop 11
	v_max3_f32 v159, v64, v65, v66
	v_max3_f32 v157, v67, v68, v69
	v_max3_f32 v158, v70, v71, v72
	v_max3_f32 v159, v159, v157, v158
	v_max3_f32 v157, v73, v74, v75
	v_max3_f32 v158, v76, v77, v78
	v_max3_f32 v157, v157, v158, v79
	v_max_f32 v159, v159, v157
	s_nop 0
	v_mov_b32_e32 v157, v159
	s_nop 1
	v_permlane32_swap_b32_e32 v159, v157
	v_max_f32 v157, v159, v157
	s_nop 0
	v_cmp_gt_f32_e32 vcc, v157, v155
	s_cbranch_vccz .LBB0_558
	v_max3_f32 v157, v155, v157, s94
	v_sub_f32_e32 v155, v155, v157
	v_exp_f32_e32 v158, v155
	v_mov_b32_e32 v155, v157
	v_mul_f32_e32 v156, v158, v156
	v_pk_mul_f32 v[14:15], v[14:15], v[158:159] op_sel_hi:[1,0]
	v_pk_mul_f32 v[12:13], v[12:13], v[158:159] op_sel_hi:[1,0]
	v_pk_mul_f32 v[10:11], v[10:11], v[158:159] op_sel_hi:[1,0]
	v_pk_mul_f32 v[8:9], v[8:9], v[158:159] op_sel_hi:[1,0]
	v_pk_mul_f32 v[6:7], v[6:7], v[158:159] op_sel_hi:[1,0]
	v_pk_mul_f32 v[4:5], v[4:5], v[158:159] op_sel_hi:[1,0]
	v_pk_mul_f32 v[2:3], v[2:3], v[158:159] op_sel_hi:[1,0]
	v_pk_mul_f32 v[0:1], v[0:1], v[158:159] op_sel_hi:[1,0]
	v_pk_mul_f32 v[30:31], v[30:31], v[158:159] op_sel_hi:[1,0]
	v_pk_mul_f32 v[28:29], v[28:29], v[158:159] op_sel_hi:[1,0]
	v_pk_mul_f32 v[26:27], v[26:27], v[158:159] op_sel_hi:[1,0]
	v_pk_mul_f32 v[24:25], v[24:25], v[158:159] op_sel_hi:[1,0]
	v_pk_mul_f32 v[22:23], v[22:23], v[158:159] op_sel_hi:[1,0]
	v_pk_mul_f32 v[20:21], v[20:21], v[158:159] op_sel_hi:[1,0]
	v_pk_mul_f32 v[18:19], v[18:19], v[158:159] op_sel_hi:[1,0]
	v_pk_mul_f32 v[16:17], v[16:17], v[158:159] op_sel_hi:[1,0]
; template <int MODE>
; __device__ __forceinline__ void attn_fox_sub(const bf16x8 (&qr)[4], f32x16& O0, f32x16& O1, float& m, float& l, unsigned saddr  , unsigned cfaddr  , int j, int kv0, int q, int hi) {
;     bf16x8 kf[4], vf[2][2]; f32x4 c0, c1, c2, c3;
;     asm volatile("ds_read_b128 %0, %12\n\tds_read_b128 %1, %12 offset:1024\n\tds_read_b128 %2, %12 offset:2048\n\tds_read_b128 %3, %12 offset:3072\n\t"
;                  "ds_read_b128 %4, %13\n\tds_read_b128 %5, %13 offset:1024\n\tds_read_b128 %6, %13 offset:2048\n\tds_read_b128 %7, %13 offset:3072\n\t"
;                  "ds_read_b128 %8, %14\n\tds_read_b128 %9, %14 offset:16\n\tds_read_b128 %10, %14 offset:64\n\tds_read_b128 %11, %14 offset:80\n\ts_waitcnt lgkmcnt(0)"
;                  : "=&v"(kf[0]), "=&v"(kf[1]), "=&v"(kf[2]), "=&v"(kf[3]), "=&v"(vf[0][0]), "=&v"(vf[0][1]), "=&v"(vf[1][0]), "=&v"(vf[1][1]), "=&v"(c0), "=&v"(c1), "=&v"(c2), "=&v"(c3)
;                  : "v"(saddr + (unsigned)j * 4096u), "v"(saddr + 8192u + (unsigned)j * 4096u), "v"(cfaddr) : "memory");
;     f32x16 S;
;     S[0] = c0[0]; S[1] = c0[1]; S[2] = c0[2]; S[3] = c0[3]; S[4] = c1[0]; S[5] = c1[1]; S[6] = c1[2]; S[7] = c1[3];
;     S[8] = c2[0]; S[9] = c2[1]; S[10] = c2[2]; S[11] = c2[3]; S[12] = c3[0]; S[13] = c3[1]; S[14] = c3[2]; S[15] = c3[3];
; #pragma unroll
;     for (int d0 = 0; d0 < 4; ++d0) S = __builtin_amdgcn_mfma_f32_32x32x16_bf16(kf[d0], qr[d0], S, 0, 0, 0);
;     if (MODE == 1) {
; #pragma unroll
;         for (int r = 0; r < 16; ++r) { const int key = kv0 + (r & 7) + 8 * hi + 16 * (r >> 3); if (key > q) S[r] = -INFINITY; }
;     }
;     float rm = rowmax16_raw(S);
;     { const auto rr = __builtin_amdgcn_permlane32_swap(__float_as_uint(rm), __float_as_uint(rm), false, false); rm = max2_raw(__uint_as_float(rr[0]), __uint_as_float(rr[1])); }
;     if (__any(rm > m)) {
;         const float mn = fmaxf(fmaxf(m, rm), -1e30f); const float alpha = __builtin_amdgcn_exp2f(m - mn);
;         l *= alpha; O0 *= alpha; O1 *= alpha; m = mn; }
;     float p[16]; float ps = 0.f;
; #pragma unroll
;     for (int r = 0; r < 16; ++r) { p[r] = __builtin_amdgcn_exp2f(S[r] - m); ps += p[r]; }
;     l += ps;
;     u32x4 w0, w1;
;     w0.x = pk2(p[0], p[1]); w0.y = pk2(p[2], p[3]); w0.z = pk2(p[4], p[5]); w0.w = pk2(p[6], p[7]);
.LBB0_558:
	s_nop 3
	v_sub_f32_e32 v66, v66, v155
	v_exp_f32_e32 v158, v66
	v_sub_f32_e32 v66, v67, v155
	v_exp_f32_e32 v67, v66
	v_sub_f32_e32 v66, v68, v155
	v_exp_f32_e32 v68, v66
	v_sub_f32_e32 v66, v69, v155
	v_sub_f32_e32 v64, v64, v155
	v_exp_f32_e32 v69, v66
	v_sub_f32_e32 v66, v70, v155
	v_exp_f32_e32 v157, v64
	v_sub_f32_e32 v65, v65, v155
	v_exp_f32_e32 v70, v66
	v_sub_f32_e32 v66, v71, v155
	v_exp_f32_e32 v65, v65
	v_exp_f32_e32 v71, v66
	v_sub_f32_e32 v66, v72, v155
	v_exp_f32_e32 v72, v66
	v_sub_f32_e32 v66, v73, v155
	v_exp_f32_e32 v73, v66
	v_sub_f32_e32 v66, v74, v155
	v_add_f32_e32 v64, 0, v157
	v_exp_f32_e32 v74, v66
	v_sub_f32_e32 v66, v75, v155
	v_add_f32_e32 v64, v65, v64
	v_exp_f32_e32 v75, v66
	v_sub_f32_e32 v66, v76, v155
	v_add_f32_e32 v64, v158, v64
	v_exp_f32_e32 v76, v66
	v_sub_f32_e32 v66, v77, v155
	v_add_f32_e32 v64, v67, v64
	v_exp_f32_e32 v77, v66
	v_sub_f32_e32 v66, v78, v155
	v_add_f32_e32 v64, v68, v64
	v_exp_f32_e32 v78, v66
	v_sub_f32_e32 v66, v79, v155
	v_add_f32_e32 v64, v69, v64
	v_exp_f32_e32 v79, v66
	v_cvt_pk_bf16_f32 v66, v157, v65
	v_cvt_pk_bf16_f32 v67, v158, v67
	v_cvt_pk_bf16_f32 v68, v68, v69
	v_cvt_pk_bf16_f32 v69, v70, v71
	v_add_f32_e32 v64, v70, v64
	v_add_f32_e32 v64, v71, v64
	s_waitcnt lgkmcnt(0)
	v_mfma_f32_32x32x16_bf16 v[0:15], v[108:111], v[66:69], v[0:15]
	v_add_f32_e32 v64, v72, v64
	v_add_f32_e32 v64, v73, v64
	v_cvt_pk_bf16_f32 v70, v72, v73
	v_cvt_pk_bf16_f32 v71, v74, v75
	v_cvt_pk_bf16_f32 v72, v76, v77
	v_cvt_pk_bf16_f32 v73, v78, v79
	v_add_f32_e32 v64, v74, v64
	v_mfma_f32_32x32x16_bf16 v[16:31], v[100:103], v[66:69], v[16:31]
	v_add_f32_e32 v64, v75, v64
	v_add_f32_e32 v64, v76, v64
	v_add_f32_e32 v64, v77, v64
	v_add_f32_e32 v64, v78, v64
	v_add_f32_e32 v64, v79, v64
	v_add_f32_e32 v64, v156, v64
	v_mfma_f32_32x32x16_bf16 v[0:15], v[104:107], v[70:73], v[0:15]
	v_mfma_f32_32x32x16_bf16 v[16:31], v[96:99], v[70:73], v[16:31]
	v_mov_b32_e32 v154, v155
	v_mov_b32_e32 v151, v64
	s_branch .LBB0_542
.LBB0_559:
	s_and_b64 vcc, exec, s[0:1]
	s_cbranch_vccz .LBB0_541
	s_andn2_b64 vcc, exec, s[2:3]
	s_mov_b64 s[0:1], -1
	s_cbranch_vccnz .LBB0_566
	v_add_u32_e32 v96, 0x1000, v131
	v_add_u32_e32 v97, 0x3000, v131
	ds_read_b128 v[48:51], v96
	ds_read_b128 v[52:55], v96 offset:1024
	ds_read_b128 v[56:59], v96 offset:2048
	ds_read_b128 v[60:63], v96 offset:3072
	ds_read_b128 v[32:35], v150
	ds_read_b128 v[36:39], v150 offset:16
	ds_read_b128 v[40:43], v150 offset:64
	ds_read_b128 v[44:47], v150 offset:80
	ds_read_b128 v[76:79], v97
	ds_read_b128 v[68:71], v97 offset:1024
	ds_read_b128 v[72:75], v97 offset:2048
	ds_read_b128 v[64:67], v97 offset:3072
	s_waitcnt lgkmcnt(4)
	v_mov_b32_e32 v155, v154
	s_nop 2
	v_mfma_f32_32x32x16_bf16 v[32:47], v[48:51], v[80:83], v[32:47]
	v_mov_b32_e32 v156, v151
	v_mfma_f32_32x32x16_bf16 v[32:47], v[52:55], v[84:87], v[32:47]
	v_mfma_f32_32x32x16_bf16 v[32:47], v[56:59], v[88:91], v[32:47]
	v_mfma_f32_32x32x16_bf16 v[32:47], v[60:63], v[92:95], v[32:47]
	s_nop 11
	v_cndmask_b32_e64 v48, v32, v140, s[20:21]
	v_cndmask_b32_e64 v111, v48, v32, s[22:23]
	v_cndmask_b32_e64 v110, v140, v33, s[22:23]
	v_cndmask_b32_e64 v109, v34, v140, s[24:25]
	v_cndmask_b32_e64 v108, v35, v140, s[26:27]
	v_cndmask_b32_e64 v107, v36, v140, s[28:29]
	v_cndmask_b32_e64 v106, v37, v140, s[30:31]
	v_cndmask_b32_e64 v105, v38, v140, s[34:35]
	v_cndmask_b32_e64 v104, v39, v140, s[36:37]
	v_cndmask_b32_e64 v103, v40, v140, s[38:39]
	v_cndmask_b32_e64 v102, v41, v140, s[40:41]
	v_cndmask_b32_e64 v101, v42, v140, s[42:43]
	v_cndmask_b32_e64 v100, v43, v140, s[44:45]
	v_cndmask_b32_e64 v99, v44, v140, s[46:47]
	v_cndmask_b32_e64 v98, v45, v140, s[48:49]
	v_cndmask_b32_e64 v97, v46, v140, s[50:51]
	v_cndmask_b32_e64 v96, v47, v140, s[52:53]
	s_nop 11
	v_max3_f32 v34, v111, v110, v109
	v_max3_f32 v32, v108, v107, v106
	v_max3_f32 v33, v105, v104, v103
	v_max3_f32 v34, v34, v32, v33
	v_max3_f32 v32, v102, v101, v100
	v_max3_f32 v33, v99, v98, v97
	v_max3_f32 v32, v32, v33, v96
	v_max_f32 v34, v34, v32
	v_mov_b64_e32 v[62:63], v[14:15]
	v_mov_b32_e32 v32, v34
	s_nop 1
	v_permlane32_swap_b32_e32 v34, v32
	v_max_f32 v157, v34, v32
	v_mov_b64_e32 v[46:47], v[30:31]
	v_cmp_gt_f32_e32 vcc, v157, v154
	v_mov_b64_e32 v[44:45], v[28:29]
	v_mov_b64_e32 v[42:43], v[26:27]
	v_mov_b64_e32 v[40:41], v[24:25]
	v_mov_b64_e32 v[38:39], v[22:23]
	v_mov_b64_e32 v[36:37], v[20:21]
	v_mov_b64_e32 v[34:35], v[18:19]
	v_mov_b64_e32 v[32:33], v[16:17]
	v_mov_b64_e32 v[60:61], v[12:13]
	v_mov_b64_e32 v[58:59], v[10:11]
	v_mov_b64_e32 v[56:57], v[8:9]
	v_mov_b64_e32 v[54:55], v[6:7]
	v_mov_b64_e32 v[52:53], v[4:5]
	v_mov_b64_e32 v[50:51], v[2:3]
	v_mov_b64_e32 v[48:49], v[0:1]
	s_cbranch_vccz .LBB0_563
	v_max3_f32 v155, v154, v157, s94
	v_sub_f32_e32 v32, v154, v155
	v_exp_f32_e32 v32, v32
	s_nop 0
	v_mul_f32_e32 v156, v151, v32
	v_pk_mul_f32 v[62:63], v[14:15], v[32:33] op_sel_hi:[1,0]
	v_pk_mul_f32 v[60:61], v[12:13], v[32:33] op_sel_hi:[1,0]
	v_pk_mul_f32 v[58:59], v[10:11], v[32:33] op_sel_hi:[1,0]
	v_pk_mul_f32 v[56:57], v[8:9], v[32:33] op_sel_hi:[1,0]
	v_pk_mul_f32 v[54:55], v[6:7], v[32:33] op_sel_hi:[1,0]
	v_pk_mul_f32 v[52:53], v[4:5], v[32:33] op_sel_hi:[1,0]
	v_pk_mul_f32 v[50:51], v[2:3], v[32:33] op_sel_hi:[1,0]
	v_pk_mul_f32 v[48:49], v[0:1], v[32:33] op_sel_hi:[1,0]
	v_pk_mul_f32 v[46:47], v[30:31], v[32:33] op_sel_hi:[1,0]
	v_pk_mul_f32 v[44:45], v[28:29], v[32:33] op_sel_hi:[1,0]
	v_pk_mul_f32 v[42:43], v[26:27], v[32:33] op_sel_hi:[1,0]
	v_pk_mul_f32 v[40:41], v[24:25], v[32:33] op_sel_hi:[1,0]
	v_pk_mul_f32 v[38:39], v[22:23], v[32:33] op_sel_hi:[1,0]
	v_pk_mul_f32 v[36:37], v[20:21], v[32:33] op_sel_hi:[1,0]
	v_pk_mul_f32 v[34:35], v[18:19], v[32:33] op_sel_hi:[1,0]
	v_pk_mul_f32 v[32:33], v[16:17], v[32:33] op_sel_hi:[1,0]
; template <int MODE>
; __device__ __forceinline__ void attn_fox_sub(const bf16x8 (&qr)[4], f32x16& O0, f32x16& O1, float& m, float& l, unsigned saddr  , unsigned cfaddr  , int j, int kv0, int q, int hi) {
;     bf16x8 kf[4], vf[2][2]; f32x4 c0, c1, c2, c3;
;     asm volatile("ds_read_b128 %0, %12\n\tds_read_b128 %1, %12 offset:1024\n\tds_read_b128 %2, %12 offset:2048\n\tds_read_b128 %3, %12 offset:3072\n\t"
;                  "ds_read_b128 %4, %13\n\tds_read_b128 %5, %13 offset:1024\n\tds_read_b128 %6, %13 offset:2048\n\tds_read_b128 %7, %13 offset:3072\n\t"
;                  "ds_read_b128 %8, %14\n\tds_read_b128 %9, %14 offset:16\n\tds_read_b128 %10, %14 offset:64\n\tds_read_b128 %11, %14 offset:80\n\ts_waitcnt lgkmcnt(0)"
;                  : "=&v"(kf[0]), "=&v"(kf[1]), "=&v"(kf[2]), "=&v"(kf[3]), "=&v"(vf[0][0]), "=&v"(vf[0][1]), "=&v"(vf[1][0]), "=&v"(vf[1][1]), "=&v"(c0), "=&v"(c1), "=&v"(c2), "=&v"(c3)
;                  : "v"(saddr + (unsigned)j * 4096u), "v"(saddr + 8192u + (unsigned)j * 4096u), "v"(cfaddr) : "memory");
;     f32x16 S;
;     S[0] = c0[0]; S[1] = c0[1]; S[2] = c0[2]; S[3] = c0[3]; S[4] = c1[0]; S[5] = c1[1]; S[6] = c1[2]; S[7] = c1[3];
;     S[8] = c2[0]; S[9] = c2[1]; S[10] = c2[2]; S[11] = c2[3]; S[12] = c3[0]; S[13] = c3[1]; S[14] = c3[2]; S[15] = c3[3];
; #pragma unroll
;     for (int d0 = 0; d0 < 4; ++d0) S = __builtin_amdgcn_mfma_f32_32x32x16_bf16(kf[d0], qr[d0], S, 0, 0, 0);
;     if (MODE == 1) {
; #pragma unroll
;         for (int r = 0; r < 16; ++r) { const int key = kv0 + (r & 7) + 8 * hi + 16 * (r >> 3); if (key > q) S[r] = -INFINITY; }
;     }
;     float rm = rowmax16_raw(S);
;     { const auto rr = __builtin_amdgcn_permlane32_swap(__float_as_uint(rm), __float_as_uint(rm), false, false); rm = max2_raw(__uint_as_float(rr[0]), __uint_as_float(rr[1])); }
;     if (__any(rm > m)) {
;         const float mn = fmaxf(fmaxf(m, rm), -1e30f); const float alpha = __builtin_amdgcn_exp2f(m - mn);
;         l *= alpha; O0 *= alpha; O1 *= alpha; m = mn; }
;     float p[16]; float ps = 0.f;
; #pragma unroll
;     for (int r = 0; r < 16; ++r) { p[r] = __builtin_amdgcn_exp2f(S[r] - m); ps += p[r]; }
;     l += ps;
;     u32x4 w0, w1;
;     w0.x = pk2(p[0], p[1]); w0.y = pk2(p[2], p[3]); w0.z = pk2(p[4], p[5]); w0.w = pk2(p[6], p[7]);
.LBB0_563:
	v_sub_f32_e32 v111, v111, v155
	v_exp_f32_e32 v111, v111
	v_sub_f32_e32 v110, v110, v155
	v_exp_f32_e32 v110, v110
	v_sub_f32_e32 v109, v109, v155
	v_exp_f32_e32 v109, v109
	v_sub_f32_e32 v108, v108, v155
	v_exp_f32_e32 v108, v108
	v_sub_f32_e32 v107, v107, v155
	v_add_f32_e32 v157, 0, v111
	v_exp_f32_e32 v107, v107
	v_sub_f32_e32 v106, v106, v155
	v_add_f32_e32 v157, v110, v157
	v_exp_f32_e32 v106, v106
	v_sub_f32_e32 v105, v105, v155
	v_add_f32_e32 v157, v109, v157
	v_exp_f32_e32 v105, v105
	v_sub_f32_e32 v104, v104, v155
	v_add_f32_e32 v157, v108, v157
	v_exp_f32_e32 v104, v104
	v_sub_f32_e32 v103, v103, v155
	v_add_f32_e32 v157, v107, v157
	v_exp_f32_e32 v103, v103
	v_sub_f32_e32 v102, v102, v155
	v_add_f32_e32 v157, v106, v157
	v_exp_f32_e32 v102, v102
	v_sub_f32_e32 v101, v101, v155
	v_add_f32_e32 v157, v105, v157
	v_exp_f32_e32 v101, v101
	v_sub_f32_e32 v100, v100, v155
	v_add_f32_e32 v157, v104, v157
	v_exp_f32_e32 v158, v100
	v_add_f32_e32 v157, v103, v157
	v_add_f32_e32 v157, v102, v157
	v_add_f32_e32 v157, v101, v157
	v_sub_f32_e32 v99, v99, v155
	v_add_f32_e32 v100, v158, v157
	v_exp_f32_e32 v157, v99
	v_sub_f32_e32 v98, v98, v155
	v_exp_f32_e32 v159, v98
	v_sub_f32_e32 v97, v97, v155
	v_exp_f32_e32 v160, v97
	v_sub_f32_e32 v96, v96, v155
	v_exp_f32_e32 v161, v96
	v_add_f32_e32 v99, v157, v100
	v_add_f32_e32 v98, v159, v99
	v_add_f32_e32 v97, v160, v98
	v_add_f32_e32 v96, v161, v97
	v_add_f32_e32 v156, v156, v96
	v_cvt_pk_bf16_f32 v96, v111, v110
	v_cvt_pk_bf16_f32 v97, v109, v108
	v_cvt_pk_bf16_f32 v98, v107, v106
	v_cvt_pk_bf16_f32 v99, v105, v104
	v_cvt_pk_bf16_f32 v100, v103, v102
	v_cvt_pk_bf16_f32 v101, v101, v158
	s_waitcnt lgkmcnt(0)
	v_mfma_f32_32x32x16_bf16 v[48:63], v[76:79], v[96:99], v[48:63]
	v_cvt_pk_bf16_f32 v102, v157, v159
	v_cvt_pk_bf16_f32 v103, v160, v161
	v_add_u32_e32 v157, 0x2000, v131
	v_mfma_f32_32x32x16_bf16 v[32:47], v[68:71], v[96:99], v[32:47]
	v_mfma_f32_32x32x16_bf16 v[48:63], v[72:75], v[100:103], v[48:63]
	v_mfma_f32_32x32x16_bf16 v[32:47], v[64:67], v[100:103], v[32:47]
	ds_read_b128 v[158:161], v131
	ds_read_b128 v[162:165], v131 offset:1024
	ds_read_b128 v[166:169], v131 offset:2048
	ds_read_b128 v[170:173], v131 offset:3072
	ds_read_b128 v[64:67], v152
	ds_read_b128 v[68:71], v152 offset:16
	ds_read_b128 v[72:75], v152 offset:64
	ds_read_b128 v[76:79], v152 offset:80
	ds_read_b128 v[108:111], v157
	ds_read_b128 v[100:103], v157 offset:1024
	ds_read_b128 v[104:107], v157 offset:2048
	ds_read_b128 v[96:99], v157 offset:3072
	s_waitcnt lgkmcnt(4)
	s_nop 0
	v_mfma_f32_32x32x16_bf16 v[64:79], v[158:161], v[80:83], v[64:79]
	v_mfma_f32_32x32x16_bf16 v[64:79], v[162:165], v[84:87], v[64:79]
	v_mfma_f32_32x32x16_bf16 v[64:79], v[166:169], v[88:91], v[64:79]
	v_mfma_f32_32x32x16_bf16 v[64:79], v[170:173], v[92:95], v[64:79]
	s_nop 11
	v_max3_f32 v159, v64, v65, v66
	v_max3_f32 v157, v67, v68, v69
	v_max3_f32 v158, v70, v71, v72
	v_max3_f32 v159, v159, v157, v158
	v_max3_f32 v157, v73, v74, v75
	v_max3_f32 v158, v76, v77, v78
	v_max3_f32 v157, v157, v158, v79
	v_max_f32 v159, v159, v157
	s_nop 0
	v_mov_b32_e32 v157, v159
	s_nop 1
	v_permlane32_swap_b32_e32 v159, v157
	v_max_f32 v157, v159, v157
	s_nop 0
	v_cmp_gt_f32_e32 vcc, v157, v155
	s_cbranch_vccz .LBB0_565
	v_max3_f32 v157, v155, v157, s94
	v_sub_f32_e32 v155, v155, v157
	v_exp_f32_e32 v158, v155
	v_mov_b32_e32 v155, v157
	v_mul_f32_e32 v156, v158, v156
	v_pk_mul_f32 v[62:63], v[62:63], v[158:159] op_sel_hi:[1,0]
	v_pk_mul_f32 v[60:61], v[60:61], v[158:159] op_sel_hi:[1,0]
	v_pk_mul_f32 v[58:59], v[58:59], v[158:159] op_sel_hi:[1,0]
	v_pk_mul_f32 v[56:57], v[56:57], v[158:159] op_sel_hi:[1,0]
	v_pk_mul_f32 v[54:55], v[54:55], v[158:159] op_sel_hi:[1,0]
	v_pk_mul_f32 v[52:53], v[52:53], v[158:159] op_sel_hi:[1,0]
	v_pk_mul_f32 v[50:51], v[50:51], v[158:159] op_sel_hi:[1,0]
	v_pk_mul_f32 v[48:49], v[48:49], v[158:159] op_sel_hi:[1,0]
	v_pk_mul_f32 v[46:47], v[46:47], v[158:159] op_sel_hi:[1,0]
	v_pk_mul_f32 v[44:45], v[44:45], v[158:159] op_sel_hi:[1,0]
	v_pk_mul_f32 v[42:43], v[42:43], v[158:159] op_sel_hi:[1,0]
	v_pk_mul_f32 v[40:41], v[40:41], v[158:159] op_sel_hi:[1,0]
	v_pk_mul_f32 v[38:39], v[38:39], v[158:159] op_sel_hi:[1,0]
	v_pk_mul_f32 v[36:37], v[36:37], v[158:159] op_sel_hi:[1,0]
	v_pk_mul_f32 v[34:35], v[34:35], v[158:159] op_sel_hi:[1,0]
	v_pk_mul_f32 v[32:33], v[32:33], v[158:159] op_sel_hi:[1,0]
; __device__ __forceinline__ unsigned pk2(float lo, float hi) { const f32x2_pk v = {lo, hi}; return __builtin_bit_cast(unsigned, __builtin_convertvector(v, bf16x2)); }
; template <int MODE>
; __device__ __forceinline__ void attn_fox_sub(const bf16x8 (&qr)[4], f32x16& O0, f32x16& O1, float& m, float& l, unsigned saddr  , unsigned cfaddr  , int j, int kv0, int q, int hi) {
;     ...
;     float p[16]; float ps = 0.f;
; #pragma unroll
;     for (int r = 0; r < 16; ++r) { p[r] = __builtin_amdgcn_exp2f(S[r] - m); ps += p[r]; }
;     l += ps;
;     u32x4 w0, w1;
;     w0.x = pk2(p[0], p[1]); w0.y = pk2(p[2], p[3]); w0.z = pk2(p[4], p[5]); w0.w = pk2(p[6], p[7]);
;     w1.x = pk2(p[8], p[9]); w1.y = pk2(p[10], p[11]); w1.z = pk2(p[12], p[13]); w1.w = pk2(p[14], p[15]);
;     const bf16x8 pf0 = __builtin_bit_cast(bf16x8, w0), pf1 = __builtin_bit_cast(bf16x8, w1);
;     O0 = __builtin_amdgcn_mfma_f32_32x32x16_bf16(vf[0][0], pf0, O0, 0, 0, 0); O0 = __builtin_amdgcn_mfma_f32_32x32x16_bf16(vf[1][0], pf1, O0, 0, 0, 0);
;     O1 = __builtin_amdgcn_mfma_f32_32x32x16_bf16(vf[0][1], pf0, O1, 0, 0, 0); O1 = __builtin_amdgcn_mfma_f32_32x32x16_bf16(vf[1][1], pf1, O1, 0, 0, 0);
; __device__ __forceinline__ void attn_fox_unit(Frame& F, const bf16_t* Qh, const bf16_t* Kh, const bf16_t* Vth, const float* CFh, const int qb, bf16_t* AOp, const float k2max) {
;     ...
;                 else attn_fox_sub<1>(qr, O0, O1, m, l, sa, cf_a + 4u * (unsigned)(64 * T), 0, 64 * T, q, hi);
.LBB0_565:
	s_nop 3
	v_sub_f32_e32 v66, v66, v155
	v_exp_f32_e32 v158, v66
	v_sub_f32_e32 v66, v67, v155
	v_exp_f32_e32 v67, v66
	v_sub_f32_e32 v66, v68, v155
	v_exp_f32_e32 v68, v66
	v_sub_f32_e32 v66, v69, v155
	v_sub_f32_e32 v64, v64, v155
	v_exp_f32_e32 v69, v66
	v_sub_f32_e32 v66, v70, v155
	v_exp_f32_e32 v157, v64
	v_sub_f32_e32 v65, v65, v155
	v_exp_f32_e32 v70, v66
	v_sub_f32_e32 v66, v71, v155
	v_exp_f32_e32 v65, v65
	v_exp_f32_e32 v71, v66
	v_sub_f32_e32 v66, v72, v155
	v_exp_f32_e32 v72, v66
	v_sub_f32_e32 v66, v73, v155
	v_exp_f32_e32 v73, v66
	v_sub_f32_e32 v66, v74, v155
	v_add_f32_e32 v64, 0, v157
	v_exp_f32_e32 v74, v66
	v_sub_f32_e32 v66, v75, v155
	v_add_f32_e32 v64, v65, v64
	v_exp_f32_e32 v75, v66
	v_sub_f32_e32 v66, v76, v155
	v_add_f32_e32 v64, v158, v64
	v_exp_f32_e32 v76, v66
	v_sub_f32_e32 v66, v77, v155
	v_add_f32_e32 v64, v67, v64
	v_exp_f32_e32 v77, v66
	v_sub_f32_e32 v66, v78, v155
	v_add_f32_e32 v64, v68, v64
	v_exp_f32_e32 v78, v66
	v_sub_f32_e32 v66, v79, v155
	v_add_f32_e32 v64, v69, v64
	v_exp_f32_e32 v79, v66
	v_cvt_pk_bf16_f32 v66, v157, v65
	v_cvt_pk_bf16_f32 v67, v158, v67
	v_cvt_pk_bf16_f32 v68, v68, v69
	v_cvt_pk_bf16_f32 v69, v70, v71
	v_add_f32_e32 v64, v70, v64
	v_add_f32_e32 v64, v71, v64
	s_waitcnt lgkmcnt(0)
	v_mfma_f32_32x32x16_bf16 v[48:63], v[108:111], v[66:69], v[48:63]
	v_add_f32_e32 v64, v72, v64
	v_add_f32_e32 v64, v73, v64
	v_cvt_pk_bf16_f32 v70, v72, v73
	v_cvt_pk_bf16_f32 v71, v74, v75
	v_cvt_pk_bf16_f32 v72, v76, v77
	v_cvt_pk_bf16_f32 v73, v78, v79
	v_add_f32_e32 v64, v74, v64
	v_mfma_f32_32x32x16_bf16 v[32:47], v[100:103], v[66:69], v[32:47]
	v_add_f32_e32 v64, v75, v64
	v_add_f32_e32 v64, v76, v64
	v_add_f32_e32 v64, v77, v64
	v_add_f32_e32 v64, v78, v64
	v_add_f32_e32 v64, v79, v64
	v_add_f32_e32 v64, v156, v64
	s_mov_b64 s[0:1], 0
	v_mfma_f32_32x32x16_bf16 v[48:63], v[104:107], v[70:73], v[48:63]
	v_mfma_f32_32x32x16_bf16 v[32:47], v[96:99], v[70:73], v[32:47]
.LBB0_566:
	s_and_b64 vcc, exec, s[0:1]
	s_cbranch_vccz .LBB0_541
	v_add_u32_e32 v96, 0x2000, v131
	ds_read_b128 v[64:67], v131
	ds_read_b128 v[68:71], v131 offset:1024
	ds_read_b128 v[72:75], v131 offset:2048
	ds_read_b128 v[76:79], v131 offset:3072
	ds_read_b128 v[32:35], v152
	ds_read_b128 v[36:39], v152 offset:16
	ds_read_b128 v[40:43], v152 offset:64
	ds_read_b128 v[44:47], v152 offset:80
	ds_read_b128 v[60:63], v96
	ds_read_b128 v[52:55], v96 offset:1024
	ds_read_b128 v[56:59], v96 offset:2048
	ds_read_b128 v[48:51], v96 offset:3072
	s_waitcnt lgkmcnt(0)
	s_nop 0
	v_mfma_f32_32x32x16_bf16 v[32:47], v[64:67], v[80:83], v[32:47]
	v_mfma_f32_32x32x16_bf16 v[32:47], v[68:71], v[84:87], v[32:47]
	v_mfma_f32_32x32x16_bf16 v[32:47], v[72:75], v[88:91], v[32:47]
	v_mfma_f32_32x32x16_bf16 v[32:47], v[76:79], v[92:95], v[32:47]
	s_nop 11
	v_cndmask_b32_e64 v71, v32, v140, s[54:55]
	v_cndmask_b32_e64 v70, v140, v33, s[56:57]
	v_cndmask_b32_e64 v69, v34, v140, s[58:59]
	v_cndmask_b32_e64 v68, v35, v140, s[60:61]
	v_cndmask_b32_e64 v67, v36, v140, s[62:63]
	v_cndmask_b32_e64 v66, v37, v140, s[64:65]
	v_cndmask_b32_e64 v65, v38, v140, s[66:67]
	v_cndmask_b32_e64 v64, v39, v140, s[68:69]
	v_cndmask_b32_e64 v40, v40, v140, s[70:71]
	v_cndmask_b32_e64 v39, v41, v140, s[72:73]
	v_cndmask_b32_e64 v38, v42, v140, s[74:75]
	v_cndmask_b32_e64 v37, v43, v140, s[76:77]
	v_cndmask_b32_e64 v36, v44, v140, s[78:79]
	v_cndmask_b32_e64 v35, v45, v140, s[80:81]
	v_cndmask_b32_e64 v34, v46, v140, s[82:83]
	v_cndmask_b32_e64 v33, v47, v140, s[84:85]
	v_cndmask_b32_e64 v32, v71, v32, s[56:57]
	s_nop 11
	v_max3_f32 v43, v32, v70, v69
	v_max3_f32 v41, v68, v67, v66
	v_max3_f32 v42, v65, v64, v40
	v_max3_f32 v43, v43, v41, v42
	v_max3_f32 v41, v39, v38, v37
	v_max3_f32 v42, v36, v35, v34
	v_max3_f32 v41, v41, v42, v33
	v_max_f32 v43, v43, v41
	s_nop 0
	v_mov_b32_e32 v41, v43
	s_nop 1
	v_permlane32_swap_b32_e32 v43, v41
	v_max_f32 v41, v43, v41
	s_nop 0
	v_cmp_gt_f32_e32 vcc, v41, v154
	s_cbranch_vccz .LBB0_540
	v_max3_f32 v41, v154, v41, s94
	v_sub_f32_e32 v42, v154, v41
	v_exp_f32_e32 v42, v42
	v_mov_b32_e32 v154, v41
	v_mul_f32_e32 v151, v151, v42
	v_pk_mul_f32 v[14:15], v[14:15], v[42:43] op_sel_hi:[1,0]
	v_pk_mul_f32 v[12:13], v[12:13], v[42:43] op_sel_hi:[1,0]
	v_pk_mul_f32 v[10:11], v[10:11], v[42:43] op_sel_hi:[1,0]
	v_pk_mul_f32 v[8:9], v[8:9], v[42:43] op_sel_hi:[1,0]
	v_pk_mul_f32 v[6:7], v[6:7], v[42:43] op_sel_hi:[1,0]
	v_pk_mul_f32 v[4:5], v[4:5], v[42:43] op_sel_hi:[1,0]
	v_pk_mul_f32 v[2:3], v[2:3], v[42:43] op_sel_hi:[1,0]
	v_pk_mul_f32 v[0:1], v[0:1], v[42:43] op_sel_hi:[1,0]
	v_pk_mul_f32 v[30:31], v[30:31], v[42:43] op_sel_hi:[1,0]
	v_pk_mul_f32 v[28:29], v[28:29], v[42:43] op_sel_hi:[1,0]
	v_pk_mul_f32 v[26:27], v[26:27], v[42:43] op_sel_hi:[1,0]
	v_pk_mul_f32 v[24:25], v[24:25], v[42:43] op_sel_hi:[1,0]
	v_pk_mul_f32 v[22:23], v[22:23], v[42:43] op_sel_hi:[1,0]
	v_pk_mul_f32 v[20:21], v[20:21], v[42:43] op_sel_hi:[1,0]
	v_pk_mul_f32 v[18:19], v[18:19], v[42:43] op_sel_hi:[1,0]
	v_pk_mul_f32 v[16:17], v[16:17], v[42:43] op_sel_hi:[1,0]
	s_branch .LBB0_540

; #define LAS __attribute__((address_space(3)))
; __device__ __forceinline__ int opaque_i(int v) { asm volatile("" : "+v"(v)); return v; }
; __device__ __forceinline__ u32x4 pack8(f32x4 a, f32x4 b) { u32x4 w; w.x = pk2(a[0], a[1]); w.y = pk2(a[2], a[3]); w.z = pk2(b[0], b[1]); w.w = pk2(b[2], b[3]); return w; }
; __device__ __forceinline__ int pi32(int i) { return (i & ~12) | ((i & 4) << 1) | ((i & 8) >> 1); }
; __device__ __forceinline__ void attn_moba_unit(Frame& F, const bf16_t* Qh, const bf16_t* Kh, const bf16_t* Vth, const float* KMh, const float slope2, const int qb, bf16_t* AOp) {
;     const int lane = opaque_i(F.lane), r32 = lane & 31, hi = lane >> 5, r32p = pi32(r32), wave = F.wave, q0 = 256 * qb + 32 * wave, q = q0 + r32;
;     LAS unsigned char* ring = F.lds; const unsigned ring_a = (unsigned)(uintptr_t)ring + 16u * (unsigned)lane;
;     bf16x8 qr[4];
; #pragma unroll
;     for (int d0 = 0; d0 < 4; ++d0) qr[d0] = *(const bf16x8*)(Qh + (size_t)q * 64 + 16 * d0 + 8 * hi);
;     f32x16 G = f32x16{};
; #pragma unroll
;     for (int d0 = 0; d0 < 4; ++d0) { u32x4 kw = {0u, 0u, 0u, 0u};
;         if (r32 < 8) { const float* kmp = KMh + r32 * 64 + 16 * d0 + 8 * hi; kw = pack8(*(const f32x4*)kmp, *(const f32x4*)(kmp + 4)); }
;         G = __builtin_amdgcn_mfma_f32_32x32x16_bf16(__builtin_bit_cast(bf16x8, kw), qr[d0], G, 0, 0, 0); }
;     float gate[8];
; #pragma unroll
;     for (int n = 0; n < 4; ++n) { const float own = G[n], oth = __shfl_xor(own, 32); gate[n] = hi ? oth : own; gate[n + 4] = hi ? own : oth; }
;     unsigned sel = 0u; const int nsel = qb < 3 ? qb : 3;
; #pragma unroll
;     for (int r = 0; r < 3; ++r) if (r < nsel) { float best = -INFINITY; int bi = 0;
; #pragma unroll
;         for (int n = 0; n < 8; ++n) if (n < qb && !((sel >> n) & 1u) && gate[n] > best) { best = gate[n]; bi = n; }
;         sel |= 1u << bi; }
.LBB0_1285:
	s_and_b32 s0, s94, 2
	v_readlane_b32 s1, v236, 35
	s_or_b32 s0, s0, s1
	s_and_b32 s1, s94, 1
	s_xor_b32 s4, s0, 7
	s_cmp_eq_u32 s1, 0
	s_cselect_b32 s10, s0, s4
	v_mov_b32_e32 v25, v208
	s_lshl_b32 s91, s10, 8
	v_readlane_b32 s0, v236, 7
	s_add_i32 s38, s91, s0
	v_and_b32_e32 v24, 31, v25
	v_ashrrev_i32_e32 v191, 5, v25
	v_or_b32_e32 v160, s38, v24
	v_readlane_b32 s0, v237, 11
	v_lshlrev_b64 v[0:1], 7, v[160:161]
	v_readlane_b32 s1, v237, 12
	v_lshlrev_b32_e32 v48, 3, v191
	v_ashrrev_i32_e32 v49, 31, v48
	v_lshl_add_u64 v[0:1], s[0:1], 0, v[0:1]
	v_lshl_add_u64 v[0:1], v[48:49], 1, v[0:1]
	global_load_dwordx4 v[128:131], v[0:1], off
	global_load_dwordx4 v[132:135], v[0:1], off offset:32
	global_load_dwordx4 v[136:139], v[0:1], off offset:64
	global_load_dwordx4 v[140:143], v[0:1], off offset:96
	v_lshlrev_b32_e32 v0, 8, v24
	v_mov_b32_e32 v1, v161
	v_lshl_add_u64 v[0:1], s[84:85], 0, v[0:1]
	v_cmp_gt_u32_e32 vcc, 8, v24
	v_lshl_add_u64 v[22:23], v[48:49], 2, v[0:1]
	v_mov_b32_e32 v16, 0
	v_mov_b32_e32 v0, 0
	v_mov_b32_e32 v1, 0
	v_mov_b32_e32 v2, 0
	v_mov_b32_e32 v3, 0
	v_mov_b32_e32 v17, 0
	v_mov_b32_e32 v18, 0
	v_mov_b32_e32 v19, 0
	v_mov_b32_e32 v96, 0
	v_mov_b32_e32 v97, 0
	v_mov_b32_e32 v98, 0
	v_mov_b32_e32 v99, 0
	v_mov_b32_e32 v100, 0
	v_mov_b32_e32 v101, 0
	v_mov_b32_e32 v102, 0
	v_mov_b32_e32 v103, 0
	s_and_saveexec_b64 s[0:1], vcc
	s_cbranch_execz .LBB0_1287
	global_load_dwordx4 v[64:67], v[22:23], off
	global_load_dwordx4 v[68:71], v[22:23], off offset:16
	global_load_dwordx4 v[72:75], v[22:23], off offset:64
	global_load_dwordx4 v[76:79], v[22:23], off offset:80
	global_load_dwordx4 v[80:83], v[22:23], off offset:128
	global_load_dwordx4 v[84:87], v[22:23], off offset:144
	global_load_dwordx4 v[88:91], v[22:23], off offset:192
	global_load_dwordx4 v[92:95], v[22:23], off offset:208
	s_waitcnt vmcnt(0)
	v_cvt_pk_bf16_f32 v0, v64, v65
	v_cvt_pk_bf16_f32 v1, v66, v67
	v_cvt_pk_bf16_f32 v2, v68, v69
	v_cvt_pk_bf16_f32 v3, v70, v71
	v_cvt_pk_bf16_f32 v16, v72, v73
	v_cvt_pk_bf16_f32 v17, v74, v75
	v_cvt_pk_bf16_f32 v18, v76, v77
	v_cvt_pk_bf16_f32 v19, v78, v79
	v_cvt_pk_bf16_f32 v96, v80, v81
	v_cvt_pk_bf16_f32 v97, v82, v83
	v_cvt_pk_bf16_f32 v98, v84, v85
	v_cvt_pk_bf16_f32 v99, v86, v87
	v_cvt_pk_bf16_f32 v100, v88, v89
	v_cvt_pk_bf16_f32 v101, v90, v91
	v_cvt_pk_bf16_f32 v102, v92, v93
	v_cvt_pk_bf16_f32 v103, v94, v95
.LBB0_1287:
	s_or_b64 exec, exec, s[0:1]
	s_waitcnt vmcnt(0)
	v_mfma_f32_32x32x16_bf16 v[0:15], v[0:3], v[128:131], 0
	v_mfma_f32_32x32x16_bf16 v[0:15], v[16:19], v[132:135], v[0:15]
	v_mfma_f32_32x32x16_bf16 v[0:15], v[96:99], v[136:139], v[0:15]
	v_mfma_f32_32x32x16_bf16 v[0:15], v[100:103], v[140:143], v[0:15]
	v_cmp_lt_i32_e32 vcc, v189, v187
	s_cmp_eq_u32 s10, 0
	s_nop 9
	v_cndmask_b32_e32 v4, v185, v189, vcc
	v_lshlrev_b32_e32 v192, 2, v4
	ds_bpermute_b32 v5, v192, v0
	ds_bpermute_b32 v6, v192, v1
	ds_bpermute_b32 v7, v192, v2
	v_cmp_gt_u32_e32 vcc, 32, v25
	s_waitcnt lgkmcnt(2)
	s_nop 0
	v_cndmask_b32_e32 v4, v5, v0, vcc
	v_cndmask_b32_e32 v0, v0, v5, vcc
	s_waitcnt lgkmcnt(1)
	v_cndmask_b32_e32 v5, v6, v1, vcc
	v_cndmask_b32_e32 v1, v1, v6, vcc
	s_waitcnt lgkmcnt(0)
	v_cndmask_b32_e32 v6, v7, v2, vcc
	v_cndmask_b32_e32 v2, v2, v7, vcc
	ds_bpermute_b32 v7, v192, v3
	s_waitcnt lgkmcnt(0)
	v_cndmask_b32_e32 v3, v7, v3, vcc
	s_cbranch_scc1 .LBB0_1340
	v_cmp_lg_f32_e32 vcc, s14, v4
	s_cmp_lg_u32 s10, 1
	s_cselect_b64 s[0:1], -1, 0
	v_cndmask_b32_e32 v7, v190, v4, vcc
	v_cmp_gt_f32_e32 vcc, v5, v7
	s_and_b64 vcc, s[0:1], vcc
	s_cmp_gt_u32 s10, 2
	v_cndmask_b32_e32 v7, v7, v5, vcc
	v_cndmask_b32_e64 v8, 0, 1, vcc
	s_cselect_b64 s[0:1], -1, 0
	v_cmp_gt_f32_e32 vcc, v6, v7
	s_and_b64 vcc, s[0:1], vcc
	s_cmp_gt_u32 s10, 3
	v_cndmask_b32_e32 v7, v7, v6, vcc
	s_cselect_b64 s[4:5], -1, 0
	v_cmp_gt_f32_e64 s[0:1], v3, v7
	s_and_b64 s[0:1], s[4:5], s[0:1]
	s_cmp_gt_u32 s10, 4
	v_cndmask_b32_e64 v7, v7, v3, s[0:1]
	s_cselect_b64 s[6:7], -1, 0
	v_cmp_gt_f32_e64 s[4:5], v0, v7
	s_and_b64 s[4:5], s[6:7], s[4:5]
	s_cmp_gt_u32 s10, 5
	v_cndmask_b32_e64 v7, v7, v0, s[4:5]
	s_cselect_b64 s[8:9], -1, 0
	v_cmp_gt_f32_e64 s[6:7], v1, v7
	s_and_b64 s[6:7], s[8:9], s[6:7]
	s_cmp_eq_u32 s10, 7
	v_cndmask_b32_e64 v7, v7, v1, s[6:7]
	v_cmp_gt_f32_e64 s[8:9], v2, v7
	v_lshlrev_b32_e64 v7, v8, 1
	v_cndmask_b32_e64 v7, v7, 4, vcc
	v_cndmask_b32_e64 v7, v7, 8, s[0:1]
	s_cselect_b64 s[12:13], -1, 0
	v_cndmask_b32_e64 v7, v7, 16, s[4:5]
	v_cndmask_b32_e64 v7, v7, 32, s[6:7]
	s_and_b64 s[0:1], s[12:13], s[8:9]
	v_cndmask_b32_e64 v193, v7, 64, s[0:1]
	s_cmp_lt_u32 s10, 2
	v_cmp_nlg_f32_e32 vcc, s14, v4
	s_cbranch_scc1 .LBB0_1296

; template <int MODE>
; __device__ __forceinline__ void attn_moba_sub(const bf16x8 (&qr)[4], f32x16& O0, f32x16& O1, float& m, float& l, unsigned saddr, int j, int kv0, int q, int q0, int hi, float slope2, bool rowok) {
;     bf16x8 kf[4], vf[2][2];
;     asm volatile("ds_read_b128 %0, %8\n\tds_read_b128 %1, %8 offset:1024\n\tds_read_b128 %2, %8 offset:2048\n\tds_read_b128 %3, %8 offset:3072\n\t"
;                  "ds_read_b128 %4, %9\n\tds_read_b128 %5, %9 offset:1024\n\tds_read_b128 %6, %9 offset:2048\n\tds_read_b128 %7, %9 offset:3072\n\ts_waitcnt lgkmcnt(0)"
;                  : "=&v"(kf[0]), "=&v"(kf[1]), "=&v"(kf[2]), "=&v"(kf[3]), "=&v"(vf[0][0]), "=&v"(vf[0][1]), "=&v"(vf[1][0]), "=&v"(vf[1][1])
;                  : "v"(saddr + (unsigned)j * 4096u), "v"(saddr + 8192u + (unsigned)j * 4096u) : "memory");
;     f32x16 S; const float sbase = slope2 * (float)(kv0 + 8 * hi - q0);
; #pragma unroll
;     for (int r = 0; r < 16; ++r) S[r] = sbase + slope2 * (float)((r & 7) + 16 * (r >> 3));
; #pragma unroll
;     for (int d0 = 0; d0 < 4; ++d0) S = __builtin_amdgcn_mfma_f32_32x32x16_bf16(kf[d0], qr[d0], S, 0, 0, 0);
;     if (MODE == 1) {
; #pragma unroll
;         for (int r = 0; r < 16; ++r) { const int key = kv0 + (r & 7) + 8 * hi + 16 * (r >> 3); if (key > q) S[r] = -INFINITY; }
;     }
;     if (MODE == 2) { if (!rowok) {
; #pragma unroll
;         for (int r = 0; r < 16; ++r) S[r] = -INFINITY; } }
;     float rm = rowmax16_raw(S);
;     { const auto rr = __builtin_amdgcn_permlane32_swap(__float_as_uint(rm), __float_as_uint(rm), false, false); rm = max2_raw(__uint_as_float(rr[0]), __uint_as_float(rr[1])); }
;     if (__any(rm > m)) { const float mn = fmaxf(fmaxf(m, rm), -1e30f); const float alpha = __builtin_amdgcn_exp2f(m - mn); l *= alpha; O0 *= alpha; O1 *= alpha; m = mn; }
;     float p[16]; float ps = 0.f;
; #pragma unroll
;     for (int r = 0; r < 16; ++r) { p[r] = __builtin_amdgcn_exp2f(S[r] - m); ps += p[r]; }
;     l += ps;
;     u32x4 w0, w1;
;     w0.x = pk2(p[0], p[1]); w0.y = pk2(p[2], p[3]); w0.z = pk2(p[4], p[5]); w0.w = pk2(p[6], p[7]);
;     w1.x = pk2(p[8], p[9]); w1.y = pk2(p[10], p[11]); w1.z = pk2(p[12], p[13]); w1.w = pk2(p[14], p[15]);
;     const bf16x8 pf0 = __builtin_bit_cast(bf16x8, w0), pf1 = __builtin_bit_cast(bf16x8, w1);
.LBB0_1309:
	v_add_u32_e32 v198, s0, v194
	s_cmp_lt_i32 s92, s78
	s_mov_b64 s[0:1], -1
	s_cbranch_scc1 .LBB0_1330
	s_cmp_lg_u32 s90, s89
	s_cbranch_scc0 .LBB0_1318
	v_mov_b64_e32 v[110:111], v[62:63]
	v_mov_b64_e32 v[94:95], v[78:79]
	s_cmp_ge_i32 s92, s87
	v_mov_b64_e32 v[108:109], v[60:61]
	v_mov_b64_e32 v[106:107], v[58:59]
	v_mov_b64_e32 v[104:105], v[56:57]
	v_mov_b64_e32 v[102:103], v[54:55]
	v_mov_b64_e32 v[100:101], v[52:53]
	v_mov_b64_e32 v[98:99], v[50:51]
	v_mov_b64_e32 v[96:97], v[48:49]
	v_mov_b64_e32 v[92:93], v[76:77]
	v_mov_b64_e32 v[90:91], v[74:75]
	v_mov_b64_e32 v[88:89], v[72:73]
	v_mov_b64_e32 v[86:87], v[70:71]
	v_mov_b64_e32 v[84:85], v[68:69]
	v_mov_b64_e32 v[82:83], v[66:67]
	v_mov_b64_e32 v[80:81], v[64:65]
	v_mov_b32_e32 v116, v197
	v_mov_b32_e32 v199, v196
	s_cbranch_scc1 .LBB0_1317
	v_add_u32_e32 v201, s89, v195
	v_add_u32_e32 v80, 0xe0, v201
	v_cvt_f32_i32_e32 v96, v80
	v_add_u32_e32 v97, 0x1000, v198
	v_add_u32_e32 v98, 0x3000, v198
	ds_read_b128 v[80:83], v97
	ds_read_b128 v[84:87], v97 offset:1024
	ds_read_b128 v[88:91], v97 offset:2048
	ds_read_b128 v[92:95], v97 offset:3072
	ds_read_b128 v[156:159], v98
	ds_read_b128 v[148:151], v98 offset:1024
	ds_read_b128 v[152:155], v98 offset:2048
	ds_read_b128 v[144:147], v98 offset:3072
	s_waitcnt lgkmcnt(4)
	v_mul_f32_e32 v96, v163, v96
	v_pk_add_f32 v[126:127], v[176:177], v[96:97] op_sel_hi:[1,0]
	v_pk_add_f32 v[124:125], v[174:175], v[96:97] op_sel_hi:[1,0]
	v_pk_add_f32 v[122:123], v[172:173], v[96:97] op_sel_hi:[1,0]
	v_pk_add_f32 v[120:121], v[170:171], v[96:97] op_sel_hi:[1,0]
	v_pk_add_f32 v[118:119], v[168:169], v[96:97] op_sel_hi:[1,0]
	v_pk_add_f32 v[116:117], v[166:167], v[96:97] op_sel_hi:[1,0]
	v_pk_add_f32 v[114:115], v[164:165], v[96:97] op_sel_hi:[1,0]
	v_pk_add_f32 v[112:113], v[162:163], v[96:97] op_sel_hi:[1,0]
	v_mov_b32_e32 v199, v196
	v_mov_b32_e32 v200, v197
	v_mfma_f32_32x32x16_bf16 v[112:127], v[80:83], v[128:131], v[112:127]
	v_mfma_f32_32x32x16_bf16 v[112:127], v[84:87], v[132:135], v[112:127]
	v_mfma_f32_32x32x16_bf16 v[112:127], v[88:91], v[136:139], v[112:127]
	v_mfma_f32_32x32x16_bf16 v[112:127], v[92:95], v[140:143], v[112:127]
	s_nop 11
	v_max3_f32 v98, v112, v113, v114
	v_max3_f32 v96, v115, v116, v117
	v_max3_f32 v97, v118, v119, v120
	v_max3_f32 v98, v98, v96, v97
	v_max3_f32 v96, v121, v122, v123
	v_max3_f32 v97, v124, v125, v126
	v_max3_f32 v96, v96, v97, v127
	v_max_f32 v98, v98, v96
	v_mov_b64_e32 v[94:95], v[78:79]
	v_mov_b32_e32 v96, v98
	s_nop 1
	v_permlane32_swap_b32_e32 v98, v96
	v_max_f32 v202, v98, v96
	v_mov_b64_e32 v[110:111], v[62:63]
	v_mov_b64_e32 v[92:93], v[76:77]
	v_mov_b64_e32 v[90:91], v[74:75]
	v_mov_b64_e32 v[88:89], v[72:73]
	v_mov_b64_e32 v[86:87], v[70:71]
	v_mov_b64_e32 v[84:85], v[68:69]
	v_mov_b64_e32 v[82:83], v[66:67]
	v_mov_b64_e32 v[80:81], v[64:65]
	v_cmp_gt_f32_e32 vcc, v202, v196
	v_mov_b64_e32 v[108:109], v[60:61]
	v_mov_b64_e32 v[106:107], v[58:59]
	v_mov_b64_e32 v[104:105], v[56:57]
	v_mov_b64_e32 v[102:103], v[54:55]
	v_mov_b64_e32 v[100:101], v[52:53]
	v_mov_b64_e32 v[98:99], v[50:51]
	v_mov_b64_e32 v[96:97], v[48:49]
	s_cbranch_vccz .LBB0_1314
	v_max3_f32 v199, v196, v202, s86
	v_sub_f32_e32 v80, v196, v199
	v_exp_f32_e32 v80, v80
	s_nop 0
	v_mul_f32_e32 v200, v197, v80
	v_pk_mul_f32 v[110:111], v[62:63], v[80:81] op_sel_hi:[1,0]
	v_pk_mul_f32 v[108:109], v[60:61], v[80:81] op_sel_hi:[1,0]
	v_pk_mul_f32 v[106:107], v[58:59], v[80:81] op_sel_hi:[1,0]
	v_pk_mul_f32 v[104:105], v[56:57], v[80:81] op_sel_hi:[1,0]
	v_pk_mul_f32 v[102:103], v[54:55], v[80:81] op_sel_hi:[1,0]
	v_pk_mul_f32 v[100:101], v[52:53], v[80:81] op_sel_hi:[1,0]
	v_pk_mul_f32 v[98:99], v[50:51], v[80:81] op_sel_hi:[1,0]
	v_pk_mul_f32 v[96:97], v[48:49], v[80:81] op_sel_hi:[1,0]
	v_pk_mul_f32 v[94:95], v[78:79], v[80:81] op_sel_hi:[1,0]
	v_pk_mul_f32 v[92:93], v[76:77], v[80:81] op_sel_hi:[1,0]
	v_pk_mul_f32 v[90:91], v[74:75], v[80:81] op_sel_hi:[1,0]
	v_pk_mul_f32 v[88:89], v[72:73], v[80:81] op_sel_hi:[1,0]
	v_pk_mul_f32 v[86:87], v[70:71], v[80:81] op_sel_hi:[1,0]
	v_pk_mul_f32 v[84:85], v[68:69], v[80:81] op_sel_hi:[1,0]
	v_pk_mul_f32 v[82:83], v[66:67], v[80:81] op_sel_hi:[1,0]
	v_pk_mul_f32 v[80:81], v[64:65], v[80:81] op_sel_hi:[1,0]
; __device__ __forceinline__ unsigned pk2(float lo, float hi) { const f32x2_pk v = {lo, hi}; return __builtin_bit_cast(unsigned, __builtin_convertvector(v, bf16x2)); }
; __device__ __forceinline__ float max2_raw(float a, float b) { float d; asm("v_max_f32 %0, %1, %2" : "=v"(d) : "v"(a), "v"(b)); return d; }
; template <int MODE>
; __device__ __forceinline__ void attn_moba_sub(const bf16x8 (&qr)[4], f32x16& O0, f32x16& O1, float& m, float& l, unsigned saddr, int j, int kv0, int q, int q0, int hi, float slope2, bool rowok) {
;     ...
;     f32x16 S; const float sbase = slope2 * (float)(kv0 + 8 * hi - q0);
; #pragma unroll
;     for (int r = 0; r < 16; ++r) S[r] = sbase + slope2 * (float)((r & 7) + 16 * (r >> 3));
; #pragma unroll
;     for (int d0 = 0; d0 < 4; ++d0) S = __builtin_amdgcn_mfma_f32_32x32x16_bf16(kf[d0], qr[d0], S, 0, 0, 0);
;     if (MODE == 1) {
; #pragma unroll
;         for (int r = 0; r < 16; ++r) { const int key = kv0 + (r & 7) + 8 * hi + 16 * (r >> 3); if (key > q) S[r] = -INFINITY; }
;     }
;     if (MODE == 2) { if (!rowok) {
; #pragma unroll
;         for (int r = 0; r < 16; ++r) S[r] = -INFINITY; } }
;     float rm = rowmax16_raw(S);
;     { const auto rr = __builtin_amdgcn_permlane32_swap(__float_as_uint(rm), __float_as_uint(rm), false, false); rm = max2_raw(__uint_as_float(rr[0]), __uint_as_float(rr[1])); }
;     if (__any(rm > m)) { const float mn = fmaxf(fmaxf(m, rm), -1e30f); const float alpha = __builtin_amdgcn_exp2f(m - mn); l *= alpha; O0 *= alpha; O1 *= alpha; m = mn; }
;     float p[16]; float ps = 0.f;
; #pragma unroll
;     for (int r = 0; r < 16; ++r) { p[r] = __builtin_amdgcn_exp2f(S[r] - m); ps += p[r]; }
;     l += ps;
;     u32x4 w0, w1;
;     w0.x = pk2(p[0], p[1]); w0.y = pk2(p[2], p[3]); w0.z = pk2(p[4], p[5]); w0.w = pk2(p[6], p[7]);
;     w1.x = pk2(p[8], p[9]); w1.y = pk2(p[10], p[11]); w1.z = pk2(p[12], p[13]); w1.w = pk2(p[14], p[15]);
;     const bf16x8 pf0 = __builtin_bit_cast(bf16x8, w0), pf1 = __builtin_bit_cast(bf16x8, w1);
;     O0 = __builtin_amdgcn_mfma_f32_32x32x16_bf16(vf[0][0], pf0, O0, 0, 0, 0); O0 = __builtin_amdgcn_mfma_f32_32x32x16_bf16(vf[1][0], pf1, O0, 0, 0, 0);
;     O1 = __builtin_amdgcn_mfma_f32_32x32x16_bf16(vf[0][1], pf0, O1, 0, 0, 0); O1 = __builtin_amdgcn_mfma_f32_32x32x16_bf16(vf[1][1], pf1, O1, 0, 0, 0);
.LBB0_1314:
	v_sub_f32_e32 v112, v112, v199
	v_exp_f32_e32 v112, v112
	v_sub_f32_e32 v113, v113, v199
	v_exp_f32_e32 v113, v113
	v_sub_f32_e32 v114, v114, v199
	v_exp_f32_e32 v114, v114
	v_sub_f32_e32 v115, v115, v199
	v_exp_f32_e32 v115, v115
	v_sub_f32_e32 v116, v116, v199
	v_add_f32_e32 v202, 0, v112
	v_exp_f32_e32 v116, v116
	v_sub_f32_e32 v117, v117, v199
	v_add_f32_e32 v202, v113, v202
	v_exp_f32_e32 v117, v117
	v_sub_f32_e32 v118, v118, v199
	v_add_f32_e32 v202, v114, v202
	v_exp_f32_e32 v118, v118
	v_sub_f32_e32 v119, v119, v199
	v_add_f32_e32 v202, v115, v202
	v_exp_f32_e32 v119, v119
	v_sub_f32_e32 v120, v120, v199
	v_add_f32_e32 v202, v116, v202
	v_exp_f32_e32 v120, v120
	v_sub_f32_e32 v121, v121, v199
	v_add_f32_e32 v202, v117, v202
	v_exp_f32_e32 v121, v121
	v_sub_f32_e32 v122, v122, v199
	v_add_f32_e32 v202, v118, v202
	v_exp_f32_e32 v122, v122
	v_sub_f32_e32 v123, v123, v199
	v_add_f32_e32 v202, v119, v202
	v_exp_f32_e32 v123, v123
	v_sub_f32_e32 v124, v124, v199
	v_cvt_pk_bf16_f32 v112, v112, v113
	v_cvt_pk_bf16_f32 v113, v114, v115
	v_cvt_pk_bf16_f32 v114, v116, v117
	v_cvt_pk_bf16_f32 v115, v118, v119
	v_add_f32_e32 v202, v120, v202
	v_exp_f32_e32 v124, v124
	v_sub_f32_e32 v125, v125, v199
	s_waitcnt lgkmcnt(0)
	v_mfma_f32_32x32x16_bf16 v[96:111], v[156:159], v[112:115], v[96:111]
	v_add_f32_e32 v202, v121, v202
	v_exp_f32_e32 v125, v125
	v_sub_f32_e32 v126, v126, v199
	v_add_f32_e32 v202, v122, v202
	v_exp_f32_e32 v126, v126
	v_sub_f32_e32 v127, v127, v199
	v_add_f32_e32 v202, v123, v202
	v_mfma_f32_32x32x16_bf16 v[80:95], v[148:151], v[112:115], v[80:95]
	v_exp_f32_e32 v127, v127
	v_add_f32_e32 v202, v124, v202
	v_add_f32_e32 v202, v125, v202
	v_add_f32_e32 v202, v126, v202
	v_add_f32_e32 v202, v127, v202
	v_cvt_pk_bf16_f32 v116, v120, v121
	v_cvt_pk_bf16_f32 v117, v122, v123
	v_cvt_pk_bf16_f32 v118, v124, v125
	v_cvt_pk_bf16_f32 v119, v126, v127
	v_add_u32_e32 v112, 0x2000, v198
	v_add_f32_e32 v200, v200, v202
	v_mfma_f32_32x32x16_bf16 v[96:111], v[152:155], v[116:119], v[96:111]
	v_mfma_f32_32x32x16_bf16 v[80:95], v[144:147], v[116:119], v[80:95]
	ds_read_b128 v[202:205], v198
	ds_read_b128 v[210:213], v198 offset:1024
	ds_read_b128 v[214:217], v198 offset:2048
	ds_read_b128 v[218:221], v198 offset:3072
	ds_read_b128 v[156:159], v112
	ds_read_b128 v[148:151], v112 offset:1024
	ds_read_b128 v[152:155], v112 offset:2048
	ds_read_b128 v[144:147], v112 offset:3072
	s_waitcnt lgkmcnt(4)
	v_add_u32_e32 v112, 0xc0, v201
	v_cvt_f32_i32_e32 v112, v112
	v_mul_f32_e32 v112, v163, v112
	v_add_f32_e64 v126, v176, v112
	v_add_f32_e64 v127, v177, v112
	v_pk_add_f32 v[124:125], v[174:175], v[112:113] op_sel_hi:[1,0]
	v_pk_add_f32 v[122:123], v[172:173], v[112:113] op_sel_hi:[1,0]
	v_pk_add_f32 v[120:121], v[170:171], v[112:113] op_sel_hi:[1,0]
	v_pk_add_f32 v[118:119], v[168:169], v[112:113] op_sel_hi:[1,0]
	v_pk_add_f32 v[116:117], v[166:167], v[112:113] op_sel_hi:[1,0]
	v_pk_add_f32 v[114:115], v[164:165], v[112:113] op_sel_hi:[1,0]
	v_pk_add_f32 v[112:113], v[162:163], v[112:113] op_sel_hi:[1,0]
	s_nop 1
	v_mfma_f32_32x32x16_bf16 v[112:127], v[202:205], v[128:131], v[112:127]
	v_mfma_f32_32x32x16_bf16 v[112:127], v[210:213], v[132:135], v[112:127]
	v_mfma_f32_32x32x16_bf16 v[112:127], v[214:217], v[136:139], v[112:127]
	v_mfma_f32_32x32x16_bf16 v[112:127], v[218:221], v[140:143], v[112:127]
	s_nop 11
	v_max3_f32 v203, v112, v113, v114
	v_max3_f32 v201, v115, v116, v117
	v_max3_f32 v202, v118, v119, v120
	v_max3_f32 v203, v203, v201, v202
	v_max3_f32 v201, v121, v122, v123
	v_max3_f32 v202, v124, v125, v126
	v_max3_f32 v201, v201, v202, v127
	v_max_f32 v203, v203, v201
	s_nop 0
	v_mov_b32_e32 v201, v203
	s_nop 1
	v_permlane32_swap_b32_e32 v203, v201
	v_max_f32 v201, v203, v201
	s_nop 0
	v_cmp_gt_f32_e32 vcc, v201, v199
	s_cbranch_vccz .LBB0_1316
	v_max3_f32 v201, v199, v201, s86
	v_sub_f32_e32 v199, v199, v201
	v_exp_f32_e32 v202, v199
	v_mov_b32_e32 v199, v201
	v_mul_f32_e32 v200, v202, v200
	v_pk_mul_f32 v[110:111], v[110:111], v[202:203] op_sel_hi:[1,0]
	v_pk_mul_f32 v[108:109], v[108:109], v[202:203] op_sel_hi:[1,0]
	v_pk_mul_f32 v[106:107], v[106:107], v[202:203] op_sel_hi:[1,0]
	v_pk_mul_f32 v[104:105], v[104:105], v[202:203] op_sel_hi:[1,0]
	v_pk_mul_f32 v[102:103], v[102:103], v[202:203] op_sel_hi:[1,0]
	v_pk_mul_f32 v[100:101], v[100:101], v[202:203] op_sel_hi:[1,0]
	v_pk_mul_f32 v[98:99], v[98:99], v[202:203] op_sel_hi:[1,0]
	v_pk_mul_f32 v[96:97], v[96:97], v[202:203] op_sel_hi:[1,0]
	v_pk_mul_f32 v[94:95], v[94:95], v[202:203] op_sel_hi:[1,0]
	v_pk_mul_f32 v[92:93], v[92:93], v[202:203] op_sel_hi:[1,0]
	v_pk_mul_f32 v[90:91], v[90:91], v[202:203] op_sel_hi:[1,0]
	v_pk_mul_f32 v[88:89], v[88:89], v[202:203] op_sel_hi:[1,0]
	v_pk_mul_f32 v[86:87], v[86:87], v[202:203] op_sel_hi:[1,0]
	v_pk_mul_f32 v[84:85], v[84:85], v[202:203] op_sel_hi:[1,0]
	v_pk_mul_f32 v[82:83], v[82:83], v[202:203] op_sel_hi:[1,0]
	v_pk_mul_f32 v[80:81], v[80:81], v[202:203] op_sel_hi:[1,0]
; __device__ __forceinline__ unsigned pk2(float lo, float hi) { const f32x2_pk v = {lo, hi}; return __builtin_bit_cast(unsigned, __builtin_convertvector(v, bf16x2)); }
; template <int MODE>
; __device__ __forceinline__ void attn_moba_sub(const bf16x8 (&qr)[4], f32x16& O0, f32x16& O1, float& m, float& l, unsigned saddr, int j, int kv0, int q, int q0, int hi, float slope2, bool rowok) {
;     ...
;     if (__any(rm > m)) { const float mn = fmaxf(fmaxf(m, rm), -1e30f); const float alpha = __builtin_amdgcn_exp2f(m - mn); l *= alpha; O0 *= alpha; O1 *= alpha; m = mn; }
;     float p[16]; float ps = 0.f;
; #pragma unroll
;     for (int r = 0; r < 16; ++r) { p[r] = __builtin_amdgcn_exp2f(S[r] - m); ps += p[r]; }
;     l += ps;
;     u32x4 w0, w1;
;     w0.x = pk2(p[0], p[1]); w0.y = pk2(p[2], p[3]); w0.z = pk2(p[4], p[5]); w0.w = pk2(p[6], p[7]);
;     w1.x = pk2(p[8], p[9]); w1.y = pk2(p[10], p[11]); w1.z = pk2(p[12], p[13]); w1.w = pk2(p[14], p[15]);
;     const bf16x8 pf0 = __builtin_bit_cast(bf16x8, w0), pf1 = __builtin_bit_cast(bf16x8, w1);
;     O0 = __builtin_amdgcn_mfma_f32_32x32x16_bf16(vf[0][0], pf0, O0, 0, 0, 0); O0 = __builtin_amdgcn_mfma_f32_32x32x16_bf16(vf[1][0], pf1, O0, 0, 0, 0);
;     O1 = __builtin_amdgcn_mfma_f32_32x32x16_bf16(vf[0][1], pf0, O1, 0, 0, 0); O1 = __builtin_amdgcn_mfma_f32_32x32x16_bf16(vf[1][1], pf1, O1, 0, 0, 0);
.LBB0_1316:
	s_nop 3
	v_sub_f32_e32 v112, v112, v199
	v_exp_f32_e32 v112, v112
	v_sub_f32_e32 v113, v113, v199
	v_exp_f32_e32 v113, v113
	v_sub_f32_e32 v114, v114, v199
	v_exp_f32_e32 v114, v114
	v_sub_f32_e32 v115, v115, v199
	v_sub_f32_e32 v116, v116, v199
	v_sub_f32_e32 v117, v117, v199
	v_sub_f32_e32 v118, v118, v199
	v_sub_f32_e32 v119, v119, v199
	v_exp_f32_e32 v115, v115
	v_exp_f32_e32 v202, v116
	v_exp_f32_e32 v117, v117
	v_exp_f32_e32 v118, v118
	v_exp_f32_e32 v119, v119
	v_add_f32_e32 v201, 0, v112
	v_add_f32_e32 v201, v113, v201
	v_add_f32_e32 v201, v114, v201
	v_add_f32_e32 v201, v115, v201
	v_cvt_pk_bf16_f32 v112, v112, v113
	v_cvt_pk_bf16_f32 v113, v114, v115
	v_cvt_pk_bf16_f32 v114, v202, v117
	v_cvt_pk_bf16_f32 v115, v118, v119
	v_sub_f32_e32 v120, v120, v199
	v_add_f32_e32 v116, v202, v201
	s_waitcnt lgkmcnt(0)
	v_mfma_f32_32x32x16_bf16 v[96:111], v[156:159], v[112:115], v[96:111]
	v_exp_f32_e32 v120, v120
	v_sub_f32_e32 v121, v121, v199
	v_sub_f32_e32 v122, v122, v199
	v_sub_f32_e32 v123, v123, v199
	v_sub_f32_e32 v124, v124, v199
	v_sub_f32_e32 v125, v125, v199
	v_sub_f32_e32 v126, v126, v199
	v_mfma_f32_32x32x16_bf16 v[80:95], v[148:151], v[112:115], v[80:95]
	v_sub_f32_e32 v127, v127, v199
	v_add_f32_e32 v116, v117, v116
	v_exp_f32_e32 v121, v121
	v_exp_f32_e32 v122, v122
	v_exp_f32_e32 v123, v123
	v_exp_f32_e32 v124, v124
	v_exp_f32_e32 v125, v125
	v_exp_f32_e32 v126, v126
	v_exp_f32_e32 v127, v127
	v_add_f32_e32 v116, v118, v116
	v_add_f32_e32 v116, v119, v116
	v_add_f32_e32 v116, v120, v116
	v_add_f32_e32 v116, v121, v116
	v_cvt_pk_bf16_f32 v118, v120, v121
	v_cvt_pk_bf16_f32 v119, v122, v123
	v_cvt_pk_bf16_f32 v120, v124, v125
	v_cvt_pk_bf16_f32 v121, v126, v127
	v_add_f32_e32 v116, v122, v116
	v_add_f32_e32 v116, v123, v116
	v_mfma_f32_32x32x16_bf16 v[96:111], v[152:155], v[118:121], v[96:111]
	v_add_f32_e32 v116, v124, v116
	v_add_f32_e32 v116, v125, v116
	v_add_f32_e32 v116, v126, v116
	v_add_f32_e32 v116, v127, v116
	v_add_f32_e32 v116, v200, v116
	v_mfma_f32_32x32x16_bf16 v[80:95], v[144:147], v[118:121], v[80:95]

; template <int MODE>
; __device__ __forceinline__ void attn_moba_sub(const bf16x8 (&qr)[4], f32x16& O0, f32x16& O1, float& m, float& l, unsigned saddr, int j, int kv0, int q, int q0, int hi, float slope2, bool rowok) {
;     bf16x8 kf[4], vf[2][2];
;     asm volatile("ds_read_b128 %0, %8\n\tds_read_b128 %1, %8 offset:1024\n\tds_read_b128 %2, %8 offset:2048\n\tds_read_b128 %3, %8 offset:3072\n\t"
;                  "ds_read_b128 %4, %9\n\tds_read_b128 %5, %9 offset:1024\n\tds_read_b128 %6, %9 offset:2048\n\tds_read_b128 %7, %9 offset:3072\n\ts_waitcnt lgkmcnt(0)"
;                  : "=&v"(kf[0]), "=&v"(kf[1]), "=&v"(kf[2]), "=&v"(kf[3]), "=&v"(vf[0][0]), "=&v"(vf[0][1]), "=&v"(vf[1][0]), "=&v"(vf[1][1])
;                  : "v"(saddr + (unsigned)j * 4096u), "v"(saddr + 8192u + (unsigned)j * 4096u) : "memory");
;     f32x16 S; const float sbase = slope2 * (float)(kv0 + 8 * hi - q0);
; #pragma unroll
;     for (int r = 0; r < 16; ++r) S[r] = sbase + slope2 * (float)((r & 7) + 16 * (r >> 3));
; #pragma unroll
;     for (int d0 = 0; d0 < 4; ++d0) S = __builtin_amdgcn_mfma_f32_32x32x16_bf16(kf[d0], qr[d0], S, 0, 0, 0);
;     if (MODE == 1) {
; #pragma unroll
;         for (int r = 0; r < 16; ++r) { const int key = kv0 + (r & 7) + 8 * hi + 16 * (r >> 3); if (key > q) S[r] = -INFINITY; }
;     }
;     if (MODE == 2) { if (!rowok) {
; #pragma unroll
;         for (int r = 0; r < 16; ++r) S[r] = -INFINITY; } }
;     float rm = rowmax16_raw(S);
;     { const auto rr = __builtin_amdgcn_permlane32_swap(__float_as_uint(rm), __float_as_uint(rm), false, false); rm = max2_raw(__uint_as_float(rr[0]), __uint_as_float(rr[1])); }
;     if (__any(rm > m)) { const float mn = fmaxf(fmaxf(m, rm), -1e30f); const float alpha = __builtin_amdgcn_exp2f(m - mn); l *= alpha; O0 *= alpha; O1 *= alpha; m = mn; }
;     float p[16]; float ps = 0.f;
; #pragma unroll
;     for (int r = 0; r < 16; ++r) { p[r] = __builtin_amdgcn_exp2f(S[r] - m); ps += p[r]; }
;     l += ps;
;     u32x4 w0, w1;
;     w0.x = pk2(p[0], p[1]); w0.y = pk2(p[2], p[3]); w0.z = pk2(p[4], p[5]); w0.w = pk2(p[6], p[7]);
;     w1.x = pk2(p[8], p[9]); w1.y = pk2(p[10], p[11]); w1.z = pk2(p[12], p[13]); w1.w = pk2(p[14], p[15]);
;     const bf16x8 pf0 = __builtin_bit_cast(bf16x8, w0), pf1 = __builtin_bit_cast(bf16x8, w1);
.LBB0_1318:
	s_andn2_b64 vcc, exec, s[0:1]
	s_cbranch_vccnz .LBB0_1329
	s_andn2_b64 vcc, exec, s[82:83]
	s_mov_b64 s[0:1], -1
	s_cbranch_vccnz .LBB0_1325
	s_nop 5
	v_add_u32_e32 v80, 0x1000, v198
	v_add_u32_e32 v81, 0x3000, v198
	ds_read_b128 v[96:99], v80
	ds_read_b128 v[100:103], v80 offset:1024
	ds_read_b128 v[104:107], v80 offset:2048
	ds_read_b128 v[108:111], v80 offset:3072
	ds_read_b128 v[124:127], v81
	ds_read_b128 v[116:119], v81 offset:1024
	ds_read_b128 v[120:123], v81 offset:2048
	ds_read_b128 v[112:115], v81 offset:3072
	s_waitcnt lgkmcnt(4)
	v_mov_b32_e32 v199, v196
	v_mfma_f32_32x32x16_bf16 v[80:95], v[96:99], v[128:131], v[0:15]
	v_mov_b32_e32 v200, v197
	v_mfma_f32_32x32x16_bf16 v[80:95], v[100:103], v[132:135], v[80:95]
	v_mfma_f32_32x32x16_bf16 v[80:95], v[104:107], v[136:139], v[80:95]
	v_mfma_f32_32x32x16_bf16 v[80:95], v[108:111], v[140:143], v[80:95]
	s_nop 11
	v_cndmask_b32_e64 v96, v80, v190, s[4:5]
	v_cndmask_b32_e64 v159, v96, v80, s[6:7]
	v_cndmask_b32_e64 v158, v190, v81, s[6:7]
	v_cndmask_b32_e64 v157, v82, v190, s[8:9]
	v_cndmask_b32_e64 v156, v83, v190, s[10:11]
	v_cndmask_b32_e64 v155, v84, v190, s[12:13]
	v_cndmask_b32_e64 v154, v85, v190, s[14:15]
	v_cndmask_b32_e64 v153, v86, v190, s[16:17]
	v_cndmask_b32_e64 v152, v87, v190, s[18:19]
	v_cndmask_b32_e64 v151, v88, v190, s[20:21]
	v_cndmask_b32_e64 v150, v89, v190, s[22:23]
	v_cndmask_b32_e64 v149, v90, v190, s[24:25]
	v_cndmask_b32_e64 v148, v91, v190, s[26:27]
	v_cndmask_b32_e64 v147, v92, v190, s[28:29]
	v_cndmask_b32_e64 v146, v93, v190, s[30:31]
	v_cndmask_b32_e64 v145, v94, v190, s[34:35]
	v_cndmask_b32_e64 v144, v95, v190, s[36:37]
	s_nop 11
	v_max3_f32 v82, v159, v158, v157
	v_max3_f32 v80, v156, v155, v154
	v_max3_f32 v81, v153, v152, v151
	v_max3_f32 v82, v82, v80, v81
	v_max3_f32 v80, v150, v149, v148
	v_max3_f32 v81, v147, v146, v145
	v_max3_f32 v80, v80, v81, v144
	v_max_f32 v82, v82, v80
	v_mov_b64_e32 v[110:111], v[62:63]
	v_mov_b32_e32 v80, v82
	s_nop 1
	v_permlane32_swap_b32_e32 v82, v80
	v_max_f32 v201, v82, v80
	v_mov_b64_e32 v[94:95], v[78:79]
	v_cmp_gt_f32_e32 vcc, v201, v196
	v_mov_b64_e32 v[92:93], v[76:77]
	v_mov_b64_e32 v[90:91], v[74:75]
	v_mov_b64_e32 v[88:89], v[72:73]
	v_mov_b64_e32 v[86:87], v[70:71]
	v_mov_b64_e32 v[84:85], v[68:69]
	v_mov_b64_e32 v[82:83], v[66:67]
	v_mov_b64_e32 v[80:81], v[64:65]
	v_mov_b64_e32 v[108:109], v[60:61]
	v_mov_b64_e32 v[106:107], v[58:59]
	v_mov_b64_e32 v[104:105], v[56:57]
	v_mov_b64_e32 v[102:103], v[54:55]
	v_mov_b64_e32 v[100:101], v[52:53]
	v_mov_b64_e32 v[98:99], v[50:51]
	v_mov_b64_e32 v[96:97], v[48:49]
	s_cbranch_vccz .LBB0_1322
	v_max3_f32 v199, v196, v201, s86
	v_sub_f32_e32 v80, v196, v199
	v_exp_f32_e32 v80, v80
	s_nop 0
	v_mul_f32_e32 v200, v197, v80
	v_pk_mul_f32 v[110:111], v[62:63], v[80:81] op_sel_hi:[1,0]
	v_pk_mul_f32 v[108:109], v[60:61], v[80:81] op_sel_hi:[1,0]
	v_pk_mul_f32 v[106:107], v[58:59], v[80:81] op_sel_hi:[1,0]
	v_pk_mul_f32 v[104:105], v[56:57], v[80:81] op_sel_hi:[1,0]
	v_pk_mul_f32 v[102:103], v[54:55], v[80:81] op_sel_hi:[1,0]
	v_pk_mul_f32 v[100:101], v[52:53], v[80:81] op_sel_hi:[1,0]
	v_pk_mul_f32 v[98:99], v[50:51], v[80:81] op_sel_hi:[1,0]
	v_pk_mul_f32 v[96:97], v[48:49], v[80:81] op_sel_hi:[1,0]
	v_pk_mul_f32 v[94:95], v[78:79], v[80:81] op_sel_hi:[1,0]
	v_pk_mul_f32 v[92:93], v[76:77], v[80:81] op_sel_hi:[1,0]
	v_pk_mul_f32 v[90:91], v[74:75], v[80:81] op_sel_hi:[1,0]
	v_pk_mul_f32 v[88:89], v[72:73], v[80:81] op_sel_hi:[1,0]
	v_pk_mul_f32 v[86:87], v[70:71], v[80:81] op_sel_hi:[1,0]
	v_pk_mul_f32 v[84:85], v[68:69], v[80:81] op_sel_hi:[1,0]
	v_pk_mul_f32 v[82:83], v[66:67], v[80:81] op_sel_hi:[1,0]
	v_pk_mul_f32 v[80:81], v[64:65], v[80:81] op_sel_hi:[1,0]
.LBB0_1322:
	v_sub_f32_e32 v159, v159, v199
	v_exp_f32_e32 v159, v159
	v_sub_f32_e32 v158, v158, v199
	v_exp_f32_e32 v158, v158
	v_sub_f32_e32 v157, v157, v199
	v_exp_f32_e32 v157, v157
	v_sub_f32_e32 v156, v156, v199
	v_exp_f32_e32 v156, v156
	v_sub_f32_e32 v155, v155, v199
	v_add_f32_e32 v201, 0, v159
	v_exp_f32_e32 v155, v155
	v_sub_f32_e32 v154, v154, v199
	v_add_f32_e32 v201, v158, v201
	v_exp_f32_e32 v154, v154
	v_sub_f32_e32 v153, v153, v199
	v_add_f32_e32 v201, v157, v201
	v_exp_f32_e32 v153, v153
	v_sub_f32_e32 v152, v152, v199
	v_add_f32_e32 v201, v156, v201
	v_exp_f32_e32 v152, v152
	v_sub_f32_e32 v151, v151, v199
	v_add_f32_e32 v201, v155, v201
	v_exp_f32_e32 v151, v151
	v_sub_f32_e32 v150, v150, v199
	v_add_f32_e32 v201, v154, v201
	v_exp_f32_e32 v150, v150
	v_sub_f32_e32 v149, v149, v199
	v_add_f32_e32 v201, v153, v201
	v_exp_f32_e32 v149, v149
	v_sub_f32_e32 v148, v148, v199
	v_add_f32_e32 v201, v152, v201
	v_exp_f32_e32 v202, v148
	v_add_f32_e32 v201, v151, v201
	v_add_f32_e32 v201, v150, v201
	v_add_f32_e32 v201, v149, v201
	v_sub_f32_e32 v147, v147, v199
	v_add_f32_e32 v148, v202, v201
	v_exp_f32_e32 v201, v147
	v_sub_f32_e32 v146, v146, v199
	v_exp_f32_e32 v203, v146
	v_sub_f32_e32 v145, v145, v199
	v_exp_f32_e32 v204, v145
	v_sub_f32_e32 v144, v144, v199
	v_exp_f32_e32 v205, v144
	v_add_f32_e32 v147, v201, v148
	v_add_f32_e32 v146, v203, v147
	v_add_f32_e32 v145, v204, v146
	v_add_f32_e32 v144, v205, v145
	v_add_f32_e32 v200, v200, v144
	v_cvt_pk_bf16_f32 v144, v159, v158
	v_cvt_pk_bf16_f32 v145, v157, v156
	v_cvt_pk_bf16_f32 v146, v155, v154
	v_cvt_pk_bf16_f32 v147, v153, v152
	v_cvt_pk_bf16_f32 v148, v151, v150
	v_cvt_pk_bf16_f32 v149, v149, v202
	s_waitcnt lgkmcnt(0)
	v_mfma_f32_32x32x16_bf16 v[80:95], v[116:119], v[144:147], v[80:95]
	v_cvt_pk_bf16_f32 v150, v201, v203
	v_cvt_pk_bf16_f32 v151, v204, v205
	v_mfma_f32_32x32x16_bf16 v[96:111], v[124:127], v[144:147], v[96:111]
	s_nop 0
	v_mfma_f32_32x32x16_bf16 v[80:95], v[112:115], v[148:151], v[80:95]
	v_add_u32_e32 v112, 0x2000, v198
	v_mfma_f32_32x32x16_bf16 v[96:111], v[120:123], v[148:151], v[96:111]
	ds_read_b128 v[202:205], v198
	ds_read_b128 v[210:213], v198 offset:1024
	ds_read_b128 v[214:217], v198 offset:2048
	ds_read_b128 v[218:221], v198 offset:3072
	ds_read_b128 v[156:159], v112
	ds_read_b128 v[148:151], v112 offset:1024
	ds_read_b128 v[152:155], v112 offset:2048
	ds_read_b128 v[144:147], v112 offset:3072
	s_waitcnt lgkmcnt(4)
	s_nop 0
	v_mfma_f32_32x32x16_bf16 v[112:127], v[202:205], v[128:131], v[16:31]
	v_mfma_f32_32x32x16_bf16 v[112:127], v[210:213], v[132:135], v[112:127]
	v_mfma_f32_32x32x16_bf16 v[112:127], v[214:217], v[136:139], v[112:127]
	v_mfma_f32_32x32x16_bf16 v[112:127], v[218:221], v[140:143], v[112:127]
	s_nop 11
	v_max3_f32 v203, v112, v113, v114
	v_max3_f32 v201, v115, v116, v117
	v_max3_f32 v202, v118, v119, v120
	v_max3_f32 v203, v203, v201, v202
	v_max3_f32 v201, v121, v122, v123
	v_max3_f32 v202, v124, v125, v126
	v_max3_f32 v201, v201, v202, v127
	v_max_f32 v203, v203, v201
	s_nop 0
	v_mov_b32_e32 v201, v203
	s_nop 1
	v_permlane32_swap_b32_e32 v203, v201
	v_max_f32 v201, v203, v201
	s_nop 0
	v_cmp_gt_f32_e32 vcc, v201, v199
	s_cbranch_vccz .LBB0_1324
; __device__ __forceinline__ unsigned pk2(float lo, float hi) { const f32x2_pk v = {lo, hi}; return __builtin_bit_cast(unsigned, __builtin_convertvector(v, bf16x2)); }
; template <int MODE>
; __device__ __forceinline__ void attn_moba_sub(const bf16x8 (&qr)[4], f32x16& O0, f32x16& O1, float& m, float& l, unsigned saddr, int j, int kv0, int q, int q0, int hi, float slope2, bool rowok) {
;     ...
;     if (__any(rm > m)) { const float mn = fmaxf(fmaxf(m, rm), -1e30f); const float alpha = __builtin_amdgcn_exp2f(m - mn); l *= alpha; O0 *= alpha; O1 *= alpha; m = mn; }
;     float p[16]; float ps = 0.f;
; #pragma unroll
;     for (int r = 0; r < 16; ++r) { p[r] = __builtin_amdgcn_exp2f(S[r] - m); ps += p[r]; }
;     l += ps;
;     u32x4 w0, w1;
;     w0.x = pk2(p[0], p[1]); w0.y = pk2(p[2], p[3]); w0.z = pk2(p[4], p[5]); w0.w = pk2(p[6], p[7]);
;     w1.x = pk2(p[8], p[9]); w1.y = pk2(p[10], p[11]); w1.z = pk2(p[12], p[13]); w1.w = pk2(p[14], p[15]);
;     const bf16x8 pf0 = __builtin_bit_cast(bf16x8, w0), pf1 = __builtin_bit_cast(bf16x8, w1);
;     O0 = __builtin_amdgcn_mfma_f32_32x32x16_bf16(vf[0][0], pf0, O0, 0, 0, 0); O0 = __builtin_amdgcn_mfma_f32_32x32x16_bf16(vf[1][0], pf1, O0, 0, 0, 0);
;     O1 = __builtin_amdgcn_mfma_f32_32x32x16_bf16(vf[0][1], pf0, O1, 0, 0, 0); O1 = __builtin_amdgcn_mfma_f32_32x32x16_bf16(vf[1][1], pf1, O1, 0, 0, 0);
	v_max3_f32 v201, v199, v201, s86
	v_sub_f32_e32 v199, v199, v201
	v_exp_f32_e32 v202, v199
	v_mov_b32_e32 v199, v201
	v_mul_f32_e32 v200, v202, v200
	v_pk_mul_f32 v[110:111], v[110:111], v[202:203] op_sel_hi:[1,0]
	v_pk_mul_f32 v[108:109], v[108:109], v[202:203] op_sel_hi:[1,0]
	v_pk_mul_f32 v[106:107], v[106:107], v[202:203] op_sel_hi:[1,0]
	v_pk_mul_f32 v[104:105], v[104:105], v[202:203] op_sel_hi:[1,0]
	v_pk_mul_f32 v[102:103], v[102:103], v[202:203] op_sel_hi:[1,0]
	v_pk_mul_f32 v[100:101], v[100:101], v[202:203] op_sel_hi:[1,0]
	v_pk_mul_f32 v[98:99], v[98:99], v[202:203] op_sel_hi:[1,0]
	v_pk_mul_f32 v[96:97], v[96:97], v[202:203] op_sel_hi:[1,0]
	v_pk_mul_f32 v[94:95], v[94:95], v[202:203] op_sel_hi:[1,0]
	v_pk_mul_f32 v[92:93], v[92:93], v[202:203] op_sel_hi:[1,0]
	v_pk_mul_f32 v[90:91], v[90:91], v[202:203] op_sel_hi:[1,0]
	v_pk_mul_f32 v[88:89], v[88:89], v[202:203] op_sel_hi:[1,0]
	v_pk_mul_f32 v[86:87], v[86:87], v[202:203] op_sel_hi:[1,0]
	v_pk_mul_f32 v[84:85], v[84:85], v[202:203] op_sel_hi:[1,0]
	v_pk_mul_f32 v[82:83], v[82:83], v[202:203] op_sel_hi:[1,0]
	v_pk_mul_f32 v[80:81], v[80:81], v[202:203] op_sel_hi:[1,0]
.LBB0_1324:
	s_nop 3
	v_sub_f32_e32 v112, v112, v199
	v_exp_f32_e32 v112, v112
	v_sub_f32_e32 v113, v113, v199
	v_exp_f32_e32 v113, v113
	v_sub_f32_e32 v114, v114, v199
	v_exp_f32_e32 v114, v114
	v_sub_f32_e32 v115, v115, v199
	v_sub_f32_e32 v116, v116, v199
	v_sub_f32_e32 v117, v117, v199
	v_sub_f32_e32 v118, v118, v199
	v_sub_f32_e32 v119, v119, v199
	v_exp_f32_e32 v115, v115
	v_exp_f32_e32 v202, v116
	v_exp_f32_e32 v117, v117
	v_exp_f32_e32 v118, v118
	v_exp_f32_e32 v119, v119
	v_add_f32_e32 v201, 0, v112
	v_add_f32_e32 v201, v113, v201
	v_add_f32_e32 v201, v114, v201
	v_add_f32_e32 v201, v115, v201
	v_cvt_pk_bf16_f32 v112, v112, v113
	v_cvt_pk_bf16_f32 v113, v114, v115
	v_cvt_pk_bf16_f32 v114, v202, v117
	v_cvt_pk_bf16_f32 v115, v118, v119
	v_sub_f32_e32 v120, v120, v199
	v_add_f32_e32 v116, v202, v201
	s_waitcnt lgkmcnt(0)
	v_mfma_f32_32x32x16_bf16 v[96:111], v[156:159], v[112:115], v[96:111]
	v_exp_f32_e32 v120, v120
	v_sub_f32_e32 v121, v121, v199
	v_sub_f32_e32 v122, v122, v199
	v_sub_f32_e32 v123, v123, v199
	v_sub_f32_e32 v124, v124, v199
	v_sub_f32_e32 v125, v125, v199
	v_sub_f32_e32 v126, v126, v199
	v_mfma_f32_32x32x16_bf16 v[80:95], v[148:151], v[112:115], v[80:95]
	v_sub_f32_e32 v127, v127, v199
	v_add_f32_e32 v116, v117, v116
	v_exp_f32_e32 v121, v121
	v_exp_f32_e32 v122, v122
	v_exp_f32_e32 v123, v123
	v_exp_f32_e32 v124, v124
	v_exp_f32_e32 v125, v125
	v_exp_f32_e32 v126, v126
	v_exp_f32_e32 v127, v127
	v_add_f32_e32 v116, v118, v116
	v_add_f32_e32 v116, v119, v116
	v_add_f32_e32 v116, v120, v116
	v_add_f32_e32 v116, v121, v116
	v_cvt_pk_bf16_f32 v118, v120, v121
	v_cvt_pk_bf16_f32 v119, v122, v123
	v_cvt_pk_bf16_f32 v120, v124, v125
	v_cvt_pk_bf16_f32 v121, v126, v127
	v_add_f32_e32 v116, v122, v116
	v_add_f32_e32 v116, v123, v116
	v_mfma_f32_32x32x16_bf16 v[96:111], v[152:155], v[118:121], v[96:111]
	v_add_f32_e32 v116, v124, v116
	v_add_f32_e32 v116, v125, v116
	v_add_f32_e32 v116, v126, v116
	v_add_f32_e32 v116, v127, v116
	v_add_f32_e32 v116, v200, v116
	s_mov_b64 s[0:1], 0
	v_mfma_f32_32x32x16_bf16 v[80:95], v[144:147], v[118:121], v[80:95]
; template <int MODE>
; __device__ __forceinline__ void attn_moba_sub(const bf16x8 (&qr)[4], f32x16& O0, f32x16& O1, float& m, float& l, unsigned saddr, int j, int kv0, int q, int q0, int hi, float slope2, bool rowok) {
;     ...
;     f32x16 S; const float sbase = slope2 * (float)(kv0 + 8 * hi - q0);
; #pragma unroll
;     for (int r = 0; r < 16; ++r) S[r] = sbase + slope2 * (float)((r & 7) + 16 * (r >> 3));
; #pragma unroll
;     for (int d0 = 0; d0 < 4; ++d0) S = __builtin_amdgcn_mfma_f32_32x32x16_bf16(kf[d0], qr[d0], S, 0, 0, 0);
;     if (MODE == 1) {
; #pragma unroll
;         for (int r = 0; r < 16; ++r) { const int key = kv0 + (r & 7) + 8 * hi + 16 * (r >> 3); if (key > q) S[r] = -INFINITY; }
;     }
;     if (MODE == 2) { if (!rowok) {
; #pragma unroll
;         for (int r = 0; r < 16; ++r) S[r] = -INFINITY; } }
;     float rm = rowmax16_raw(S);
;     { const auto rr = __builtin_amdgcn_permlane32_swap(__float_as_uint(rm), __float_as_uint(rm), false, false); rm = max2_raw(__uint_as_float(rr[0]), __uint_as_float(rr[1])); }
;     if (__any(rm > m)) { const float mn = fmaxf(fmaxf(m, rm), -1e30f); const float alpha = __builtin_amdgcn_exp2f(m - mn); l *= alpha; O0 *= alpha; O1 *= alpha; m = mn; }
;     float p[16]; float ps = 0.f;
; #pragma unroll
;     for (int r = 0; r < 16; ++r) { p[r] = __builtin_amdgcn_exp2f(S[r] - m); ps += p[r]; }
;     l += ps;
;     u32x4 w0, w1;
;     w0.x = pk2(p[0], p[1]); w0.y = pk2(p[2], p[3]); w0.z = pk2(p[4], p[5]); w0.w = pk2(p[6], p[7]);
;     w1.x = pk2(p[8], p[9]); w1.y = pk2(p[10], p[11]); w1.z = pk2(p[12], p[13]); w1.w = pk2(p[14], p[15]);
;     const bf16x8 pf0 = __builtin_bit_cast(bf16x8, w0), pf1 = __builtin_bit_cast(bf16x8, w1);
;     O0 = __builtin_amdgcn_mfma_f32_32x32x16_bf16(vf[0][0], pf0, O0, 0, 0, 0); O0 = __builtin_amdgcn_mfma_f32_32x32x16_bf16(vf[1][0], pf1, O0, 0, 0, 0);
;     O1 = __builtin_amdgcn_mfma_f32_32x32x16_bf16(vf[0][1], pf0, O1, 0, 0, 0); O1 = __builtin_amdgcn_mfma_f32_32x32x16_bf16(vf[1][1], pf1, O1, 0, 0, 0);
; __device__ __forceinline__ void attn_moba_unit(Frame& F, const bf16_t* Qh, const bf16_t* Kh, const bf16_t* Vth, const float* KMh, const float slope2, const int qb, bf16_t* AOp) {
;     ...
;                 else attn_moba_sub<1>(qr, O0, O1, m, l, sa, 0, 64 * T, q, q0, hi, slope2, true);
.LBB0_1325:
	s_and_b64 vcc, exec, s[0:1]
	s_cbranch_vccz .LBB0_1329
	s_nop 9
	v_add_u32_e32 v80, 0x2000, v198
	ds_read_b128 v[96:99], v198
	ds_read_b128 v[100:103], v198 offset:1024
	ds_read_b128 v[104:107], v198 offset:2048
	ds_read_b128 v[108:111], v198 offset:3072
	ds_read_b128 v[124:127], v80
	ds_read_b128 v[116:119], v80 offset:1024
	ds_read_b128 v[120:123], v80 offset:2048
	ds_read_b128 v[112:115], v80 offset:3072
	s_waitcnt lgkmcnt(4)
	v_mov_b32_e32 v199, v196
	v_mfma_f32_32x32x16_bf16 v[80:95], v[96:99], v[128:131], v[32:47]
	v_mov_b32_e32 v200, v197
	v_mfma_f32_32x32x16_bf16 v[80:95], v[100:103], v[132:135], v[80:95]
	v_mfma_f32_32x32x16_bf16 v[80:95], v[104:107], v[136:139], v[80:95]
	v_mfma_f32_32x32x16_bf16 v[80:95], v[108:111], v[140:143], v[80:95]
	s_nop 11
	v_cndmask_b32_e64 v96, v80, v190, s[38:39]
	v_cndmask_b32_e64 v159, v96, v80, s[40:41]
	v_cndmask_b32_e64 v158, v190, v81, s[40:41]
	v_cndmask_b32_e64 v157, v82, v190, s[42:43]
	v_cndmask_b32_e64 v156, v83, v190, s[44:45]
	v_cndmask_b32_e64 v155, v84, v190, s[46:47]
	v_cndmask_b32_e64 v154, v85, v190, s[48:49]
	v_cndmask_b32_e64 v153, v86, v190, s[50:51]
	v_cndmask_b32_e64 v152, v87, v190, s[52:53]
	v_cndmask_b32_e64 v151, v88, v190, s[54:55]
	v_cndmask_b32_e64 v150, v89, v190, s[56:57]
	v_cndmask_b32_e64 v149, v90, v190, s[58:59]
	v_cndmask_b32_e64 v148, v91, v190, s[60:61]
	v_cndmask_b32_e64 v147, v92, v190, s[62:63]
	v_cndmask_b32_e64 v146, v93, v190, s[64:65]
	v_cndmask_b32_e64 v145, v94, v190, s[66:67]
	v_cndmask_b32_e64 v144, v95, v190, s[68:69]
	s_nop 11
	v_max3_f32 v82, v159, v158, v157
	v_max3_f32 v80, v156, v155, v154
	v_max3_f32 v81, v153, v152, v151
	v_max3_f32 v82, v82, v80, v81
	v_max3_f32 v80, v150, v149, v148
	v_max3_f32 v81, v147, v146, v145
	v_max3_f32 v80, v80, v81, v144
	v_max_f32 v82, v82, v80
	v_mov_b64_e32 v[110:111], v[62:63]
	v_mov_b32_e32 v80, v82
	s_nop 1
	v_permlane32_swap_b32_e32 v82, v80
	v_max_f32 v201, v82, v80
	v_mov_b64_e32 v[94:95], v[78:79]
	v_cmp_gt_f32_e32 vcc, v201, v196
	v_mov_b64_e32 v[92:93], v[76:77]
	v_mov_b64_e32 v[90:91], v[74:75]
	v_mov_b64_e32 v[88:89], v[72:73]
	v_mov_b64_e32 v[86:87], v[70:71]
	v_mov_b64_e32 v[84:85], v[68:69]
	v_mov_b64_e32 v[82:83], v[66:67]
	v_mov_b64_e32 v[80:81], v[64:65]
	v_mov_b64_e32 v[108:109], v[60:61]
	v_mov_b64_e32 v[106:107], v[58:59]
	v_mov_b64_e32 v[104:105], v[56:57]
	v_mov_b64_e32 v[102:103], v[54:55]
	v_mov_b64_e32 v[100:101], v[52:53]
	v_mov_b64_e32 v[98:99], v[50:51]
	v_mov_b64_e32 v[96:97], v[48:49]
	s_cbranch_vccz .LBB0_1328
	v_max3_f32 v199, v196, v201, s86
	v_sub_f32_e32 v80, v196, v199
	v_exp_f32_e32 v80, v80
	s_nop 0
	v_mul_f32_e32 v200, v197, v80
	v_pk_mul_f32 v[110:111], v[62:63], v[80:81] op_sel_hi:[1,0]
	v_pk_mul_f32 v[108:109], v[60:61], v[80:81] op_sel_hi:[1,0]
	v_pk_mul_f32 v[106:107], v[58:59], v[80:81] op_sel_hi:[1,0]
	v_pk_mul_f32 v[104:105], v[56:57], v[80:81] op_sel_hi:[1,0]
	v_pk_mul_f32 v[102:103], v[54:55], v[80:81] op_sel_hi:[1,0]
	v_pk_mul_f32 v[100:101], v[52:53], v[80:81] op_sel_hi:[1,0]
	v_pk_mul_f32 v[98:99], v[50:51], v[80:81] op_sel_hi:[1,0]
	v_pk_mul_f32 v[96:97], v[48:49], v[80:81] op_sel_hi:[1,0]
	v_pk_mul_f32 v[94:95], v[78:79], v[80:81] op_sel_hi:[1,0]
	v_pk_mul_f32 v[92:93], v[76:77], v[80:81] op_sel_hi:[1,0]
	v_pk_mul_f32 v[90:91], v[74:75], v[80:81] op_sel_hi:[1,0]
	v_pk_mul_f32 v[88:89], v[72:73], v[80:81] op_sel_hi:[1,0]
	v_pk_mul_f32 v[86:87], v[70:71], v[80:81] op_sel_hi:[1,0]
	v_pk_mul_f32 v[84:85], v[68:69], v[80:81] op_sel_hi:[1,0]
	v_pk_mul_f32 v[82:83], v[66:67], v[80:81] op_sel_hi:[1,0]
	v_pk_mul_f32 v[80:81], v[64:65], v[80:81] op_sel_hi:[1,0]
.LBB0_1328:
	v_sub_f32_e32 v159, v159, v199
	v_sub_f32_e32 v158, v158, v199
	v_sub_f32_e32 v157, v157, v199
	v_sub_f32_e32 v156, v156, v199
	v_sub_f32_e32 v155, v155, v199
	v_sub_f32_e32 v154, v154, v199
	v_sub_f32_e32 v153, v153, v199
	v_sub_f32_e32 v152, v152, v199
	v_exp_f32_e32 v159, v159
	v_exp_f32_e32 v158, v158
	v_exp_f32_e32 v157, v157
	v_exp_f32_e32 v156, v156
	v_exp_f32_e32 v155, v155
	v_exp_f32_e32 v154, v154
	v_exp_f32_e32 v153, v153
	v_exp_f32_e32 v152, v152
	v_sub_f32_e32 v149, v149, v199
	v_sub_f32_e32 v148, v148, v199
	v_sub_f32_e32 v147, v147, v199
	v_sub_f32_e32 v146, v146, v199
	v_exp_f32_e32 v202, v149
	v_exp_f32_e32 v203, v148
	v_exp_f32_e32 v204, v147
	v_exp_f32_e32 v205, v146
	v_cvt_pk_bf16_f32 v146, v159, v158
	v_cvt_pk_bf16_f32 v147, v157, v156
	v_cvt_pk_bf16_f32 v148, v155, v154
	v_cvt_pk_bf16_f32 v149, v153, v152
	v_sub_f32_e32 v151, v151, v199
	v_sub_f32_e32 v150, v150, v199
	s_waitcnt lgkmcnt(0)
	v_mfma_f32_32x32x16_bf16 v[96:111], v[124:127], v[146:149], v[96:111]
	v_sub_f32_e32 v145, v145, v199
	v_sub_f32_e32 v124, v144, v199
	v_exp_f32_e32 v151, v151
	v_exp_f32_e32 v150, v150
	v_exp_f32_e32 v145, v145
	v_exp_f32_e32 v144, v124
	v_add_f32_e32 v201, 0, v159
	v_add_f32_e32 v201, v158, v201
	v_mfma_f32_32x32x16_bf16 v[80:95], v[116:119], v[146:149], v[80:95]
	v_add_f32_e32 v201, v157, v201
	v_cvt_pk_bf16_f32 v124, v151, v150
	v_cvt_pk_bf16_f32 v125, v202, v203
	v_cvt_pk_bf16_f32 v126, v204, v205
	v_cvt_pk_bf16_f32 v127, v145, v144
	s_nop 1
	v_mfma_f32_32x32x16_bf16 v[96:111], v[120:123], v[124:127], v[96:111]
	v_add_f32_e32 v120, v156, v201
	v_add_f32_e32 v120, v155, v120
	v_add_f32_e32 v120, v154, v120
	v_add_f32_e32 v120, v153, v120
	v_add_f32_e32 v120, v152, v120
	v_add_f32_e32 v120, v151, v120
	v_add_f32_e32 v120, v150, v120
	v_mfma_f32_32x32x16_bf16 v[80:95], v[112:115], v[124:127], v[80:95]
	v_add_f32_e32 v116, v202, v120
	v_add_f32_e32 v116, v203, v116
	v_add_f32_e32 v116, v204, v116
	v_add_f32_e32 v116, v205, v116
	v_add_f32_e32 v116, v145, v116
	v_add_f32_e32 v116, v144, v116
	v_add_f32_e32 v116, v200, v116

; template <int MODE>
; __device__ __forceinline__ void attn_moba_sub(const bf16x8 (&qr)[4], f32x16& O0, f32x16& O1, float& m, float& l, unsigned saddr, int j, int kv0, int q, int q0, int hi, float slope2, bool rowok) {
;     bf16x8 kf[4], vf[2][2];
;     asm volatile("ds_read_b128 %0, %8\n\tds_read_b128 %1, %8 offset:1024\n\tds_read_b128 %2, %8 offset:2048\n\tds_read_b128 %3, %8 offset:3072\n\t"
;                  "ds_read_b128 %4, %9\n\tds_read_b128 %5, %9 offset:1024\n\tds_read_b128 %6, %9 offset:2048\n\tds_read_b128 %7, %9 offset:3072\n\ts_waitcnt lgkmcnt(0)"
;                  : "=&v"(kf[0]), "=&v"(kf[1]), "=&v"(kf[2]), "=&v"(kf[3]), "=&v"(vf[0][0]), "=&v"(vf[0][1]), "=&v"(vf[1][0]), "=&v"(vf[1][1])
;                  : "v"(saddr + (unsigned)j * 4096u), "v"(saddr + 8192u + (unsigned)j * 4096u) : "memory");
;     f32x16 S; const float sbase = slope2 * (float)(kv0 + 8 * hi - q0);
; #pragma unroll
;     for (int r = 0; r < 16; ++r) S[r] = sbase + slope2 * (float)((r & 7) + 16 * (r >> 3));
; #pragma unroll
;     for (int d0 = 0; d0 < 4; ++d0) S = __builtin_amdgcn_mfma_f32_32x32x16_bf16(kf[d0], qr[d0], S, 0, 0, 0);
;     if (MODE == 1) {
; #pragma unroll
;         for (int r = 0; r < 16; ++r) { const int key = kv0 + (r & 7) + 8 * hi + 16 * (r >> 3); if (key > q) S[r] = -INFINITY; }
;     }
;     if (MODE == 2) { if (!rowok) {
; #pragma unroll
;         for (int r = 0; r < 16; ++r) S[r] = -INFINITY; } }
;     float rm = rowmax16_raw(S);
;     { const auto rr = __builtin_amdgcn_permlane32_swap(__float_as_uint(rm), __float_as_uint(rm), false, false); rm = max2_raw(__uint_as_float(rr[0]), __uint_as_float(rr[1])); }
;     if (__any(rm > m)) { const float mn = fmaxf(fmaxf(m, rm), -1e30f); const float alpha = __builtin_amdgcn_exp2f(m - mn); l *= alpha; O0 *= alpha; O1 *= alpha; m = mn; }
; __device__ __forceinline__ void attn_moba_unit(Frame& F, const bf16_t* Qh, const bf16_t* Kh, const bf16_t* Vth, const float* KMh, const float slope2, const int qb, bf16_t* AOp) {
;     ...
;         } else if ((wsel >> (T >> 2)) & 1u) {
;             const bool rowok = (sel >> (T >> 2)) & 1u;
;             attn_moba_sub<2>(qr, O0, O1, m, l, sa, 1, 64 * T + 32, q, q0, hi, slope2, rowok); attn_moba_sub<2>(qr, O0, O1, m, l, sa, 0, 64 * T, q, q0, hi, slope2, rowok);
.LBB0_1331:
	s_lshr_b32 s0, s92, 2
	s_lshl_b32 s0, 1, s0
	s_and_b32 s1, s0, s79
	s_cmp_eq_u32 s1, 0
	s_cbranch_scc1 .LBB0_1337
	v_add_u32_e32 v113, s89, v195
	s_nop 1
	v_add_u32_e32 v80, 0xe0, v113
	v_cvt_f32_i32_e32 v80, v80
	v_add_u32_e32 v81, 0x1000, v198
	v_add_u32_e32 v82, 0x3000, v198
	ds_read_b128 v[114:117], v81
	ds_read_b128 v[118:121], v81 offset:1024
	ds_read_b128 v[122:125], v81 offset:2048
	ds_read_b128 v[144:147], v81 offset:3072
	ds_read_b128 v[108:111], v82
	ds_read_b128 v[100:103], v82 offset:1024
	ds_read_b128 v[104:107], v82 offset:2048
	ds_read_b128 v[96:99], v82 offset:3072
	s_waitcnt lgkmcnt(4)
	v_mul_f32_e32 v80, v163, v80
	v_pk_add_f32 v[94:95], v[176:177], v[80:81] op_sel_hi:[1,0]
	v_pk_add_f32 v[92:93], v[174:175], v[80:81] op_sel_hi:[1,0]
	v_pk_add_f32 v[90:91], v[172:173], v[80:81] op_sel_hi:[1,0]
	v_pk_add_f32 v[88:89], v[170:171], v[80:81] op_sel_hi:[1,0]
	v_pk_add_f32 v[86:87], v[168:169], v[80:81] op_sel_hi:[1,0]
	v_pk_add_f32 v[84:85], v[166:167], v[80:81] op_sel_hi:[1,0]
	v_pk_add_f32 v[82:83], v[164:165], v[80:81] op_sel_hi:[1,0]
	v_pk_add_f32 v[80:81], v[162:163], v[80:81] op_sel_hi:[1,0]
	v_and_b32_e32 v112, s0, v193
	v_cmp_eq_u32_e64 s[70:71], 0, v112
	v_mfma_f32_32x32x16_bf16 v[80:95], v[114:117], v[128:131], v[80:95]
	v_mfma_f32_32x32x16_bf16 v[80:95], v[118:121], v[132:135], v[80:95]
	v_mfma_f32_32x32x16_bf16 v[80:95], v[122:125], v[136:139], v[80:95]
	v_mfma_f32_32x32x16_bf16 v[80:95], v[144:147], v[140:143], v[80:95]
	s_nop 11
	v_cndmask_b32_e64 v120, v80, v190, s[70:71]
	v_cndmask_b32_e64 v119, v81, v190, s[70:71]
	v_cndmask_b32_e64 v118, v82, v190, s[70:71]
	v_cndmask_b32_e64 v117, v83, v190, s[70:71]
	v_cndmask_b32_e64 v116, v84, v190, s[70:71]
	v_cndmask_b32_e64 v115, v85, v190, s[70:71]
	v_cndmask_b32_e64 v114, v86, v190, s[70:71]
	v_cndmask_b32_e64 v112, v87, v190, s[70:71]
	v_cndmask_b32_e64 v87, v88, v190, s[70:71]
	v_cndmask_b32_e64 v86, v89, v190, s[70:71]
	v_cndmask_b32_e64 v85, v90, v190, s[70:71]
	v_cndmask_b32_e64 v84, v91, v190, s[70:71]
	v_cndmask_b32_e64 v83, v92, v190, s[70:71]
	v_cndmask_b32_e64 v82, v93, v190, s[70:71]
	v_cndmask_b32_e64 v81, v94, v190, s[70:71]
	v_cndmask_b32_e64 v80, v95, v190, s[70:71]
	s_nop 11
	v_max3_f32 v90, v120, v119, v118
	v_max3_f32 v88, v117, v116, v115
	v_max3_f32 v89, v114, v112, v87
	v_max3_f32 v90, v90, v88, v89
	v_max3_f32 v88, v86, v85, v84
	v_max3_f32 v89, v83, v82, v81
	v_max3_f32 v88, v88, v89, v80
	v_max_f32 v90, v90, v88
	s_nop 0
	v_mov_b32_e32 v88, v90
	s_nop 1
	v_permlane32_swap_b32_e32 v90, v88
	v_max_f32 v88, v90, v88
	s_nop 0
	v_cmp_gt_f32_e32 vcc, v88, v196
	s_cbranch_vccz .LBB0_1334
	v_max3_f32 v89, v196, v88, s86
	v_sub_f32_e32 v88, v196, v89
	v_exp_f32_e32 v88, v88
	v_mov_b32_e32 v196, v89
	v_mul_f32_e32 v197, v197, v88
	v_pk_mul_f32 v[62:63], v[62:63], v[88:89] op_sel_hi:[1,0]
	v_pk_mul_f32 v[60:61], v[60:61], v[88:89] op_sel_hi:[1,0]
	v_pk_mul_f32 v[58:59], v[58:59], v[88:89] op_sel_hi:[1,0]
	v_pk_mul_f32 v[56:57], v[56:57], v[88:89] op_sel_hi:[1,0]
	v_pk_mul_f32 v[54:55], v[54:55], v[88:89] op_sel_hi:[1,0]
	v_pk_mul_f32 v[52:53], v[52:53], v[88:89] op_sel_hi:[1,0]
	v_pk_mul_f32 v[50:51], v[50:51], v[88:89] op_sel_hi:[1,0]
	v_pk_mul_f32 v[48:49], v[48:49], v[88:89] op_sel_hi:[1,0]
	v_pk_mul_f32 v[78:79], v[78:79], v[88:89] op_sel_hi:[1,0]
	v_pk_mul_f32 v[76:77], v[76:77], v[88:89] op_sel_hi:[1,0]
	v_pk_mul_f32 v[74:75], v[74:75], v[88:89] op_sel_hi:[1,0]
	v_pk_mul_f32 v[72:73], v[72:73], v[88:89] op_sel_hi:[1,0]
	v_pk_mul_f32 v[70:71], v[70:71], v[88:89] op_sel_hi:[1,0]
	v_pk_mul_f32 v[68:69], v[68:69], v[88:89] op_sel_hi:[1,0]
	v_pk_mul_f32 v[66:67], v[66:67], v[88:89] op_sel_hi:[1,0]
	v_pk_mul_f32 v[64:65], v[64:65], v[88:89] op_sel_hi:[1,0]
.LBB0_1334:
	v_sub_f32_e32 v88, v120, v196
	v_exp_f32_e32 v88, v88
	v_sub_f32_e32 v90, v119, v196
	v_exp_f32_e32 v90, v90
	v_sub_f32_e32 v91, v118, v196
	v_exp_f32_e32 v91, v91
	v_sub_f32_e32 v92, v117, v196
	v_exp_f32_e32 v92, v92
	v_sub_f32_e32 v93, v116, v196
	v_add_f32_e32 v89, 0, v88
	v_exp_f32_e32 v93, v93
	v_sub_f32_e32 v94, v115, v196
	v_add_f32_e32 v89, v90, v89
	v_exp_f32_e32 v94, v94
	v_sub_f32_e32 v95, v114, v196
	v_add_f32_e32 v89, v91, v89
	v_exp_f32_e32 v95, v95
	v_sub_f32_e32 v112, v112, v196
	v_add_f32_e32 v89, v92, v89
	v_exp_f32_e32 v114, v112
	v_sub_f32_e32 v87, v87, v196
	v_add_f32_e32 v89, v93, v89
	v_exp_f32_e32 v87, v87
	v_sub_f32_e32 v86, v86, v196
	v_add_f32_e32 v89, v94, v89
	v_exp_f32_e32 v86, v86
	v_sub_f32_e32 v85, v85, v196
	v_add_f32_e32 v89, v95, v89
	v_exp_f32_e32 v85, v85
	v_sub_f32_e32 v84, v84, v196
	v_add_f32_e32 v89, v114, v89
	v_exp_f32_e32 v115, v84
	v_add_f32_e32 v89, v87, v89
	v_add_f32_e32 v89, v86, v89
	v_add_f32_e32 v89, v85, v89
	v_sub_f32_e32 v83, v83, v196
	v_add_f32_e32 v84, v115, v89
	v_exp_f32_e32 v89, v83
	v_sub_f32_e32 v82, v82, v196
	v_exp_f32_e32 v116, v82
	v_sub_f32_e32 v81, v81, v196
	v_exp_f32_e32 v117, v81
	v_sub_f32_e32 v80, v80, v196
	v_exp_f32_e32 v118, v80
	v_add_f32_e32 v83, v89, v84
	v_add_f32_e32 v82, v116, v83
	v_add_f32_e32 v81, v117, v82
	v_add_f32_e32 v80, v118, v81
	v_add_f32_e32 v112, v197, v80
	v_cvt_pk_bf16_f32 v80, v88, v90
	v_cvt_pk_bf16_f32 v81, v91, v92
	v_cvt_pk_bf16_f32 v82, v93, v94
	v_cvt_pk_bf16_f32 v83, v95, v114
	v_cvt_pk_bf16_f32 v84, v87, v86
	v_cvt_pk_bf16_f32 v85, v85, v115
	s_waitcnt lgkmcnt(0)
; __device__ __forceinline__ unsigned pk2(float lo, float hi) { const f32x2_pk v = {lo, hi}; return __builtin_bit_cast(unsigned, __builtin_convertvector(v, bf16x2)); }
; template <int MODE>
; __device__ __forceinline__ void attn_moba_sub(const bf16x8 (&qr)[4], f32x16& O0, f32x16& O1, float& m, float& l, unsigned saddr, int j, int kv0, int q, int q0, int hi, float slope2, bool rowok) {
;     ...
;     if (__any(rm > m)) { const float mn = fmaxf(fmaxf(m, rm), -1e30f); const float alpha = __builtin_amdgcn_exp2f(m - mn); l *= alpha; O0 *= alpha; O1 *= alpha; m = mn; }
;     float p[16]; float ps = 0.f;
; #pragma unroll
;     for (int r = 0; r < 16; ++r) { p[r] = __builtin_amdgcn_exp2f(S[r] - m); ps += p[r]; }
;     l += ps;
;     u32x4 w0, w1;
;     w0.x = pk2(p[0], p[1]); w0.y = pk2(p[2], p[3]); w0.z = pk2(p[4], p[5]); w0.w = pk2(p[6], p[7]);
;     w1.x = pk2(p[8], p[9]); w1.y = pk2(p[10], p[11]); w1.z = pk2(p[12], p[13]); w1.w = pk2(p[14], p[15]);
;     const bf16x8 pf0 = __builtin_bit_cast(bf16x8, w0), pf1 = __builtin_bit_cast(bf16x8, w1);
;     O0 = __builtin_amdgcn_mfma_f32_32x32x16_bf16(vf[0][0], pf0, O0, 0, 0, 0); O0 = __builtin_amdgcn_mfma_f32_32x32x16_bf16(vf[1][0], pf1, O0, 0, 0, 0);
;     O1 = __builtin_amdgcn_mfma_f32_32x32x16_bf16(vf[0][1], pf0, O1, 0, 0, 0); O1 = __builtin_amdgcn_mfma_f32_32x32x16_bf16(vf[1][1], pf1, O1, 0, 0, 0);
; __device__ __forceinline__ void attn_moba_unit(Frame& F, const bf16_t* Qh, const bf16_t* Kh, const bf16_t* Vth, const float* KMh, const float slope2, const int qb, bf16_t* AOp) {
;     ...
; #pragma unroll 1
;     for (int T = NT - 1; T >= 0; --T) {
;         if (T >= 2) asm volatile("s_waitcnt vmcnt(4)" ::: "memory"); else if (T == 1) asm volatile("s_waitcnt vmcnt(2)" ::: "memory"); else asm volatile("s_waitcnt vmcnt(0)" ::: "memory");
;         __builtin_amdgcn_s_barrier();
;         if (T >= 3) { const int fs = (slot + 3) & 3; attn_dma_tile(Kh, Vth, T - 3, ring + fs * AT_SLOT, wave, r32, r32p, hi); }
;         const unsigned sa = ring_a + (unsigned)(slot * AT_SLOT);
;         if (T >= 4 * qb) {
;             if (T == my_last) {
;                 if (jdiag == 1) { attn_moba_sub<1>(qr, O0, O1, m, l, sa, 1, 64 * T + 32, q, q0, hi, slope2, true); attn_moba_sub<0>(qr, O0, O1, m, l, sa, 0, 64 * T, q, q0, hi, slope2, true); }
;                 else attn_moba_sub<1>(qr, O0, O1, m, l, sa, 0, 64 * T, q, q0, hi, slope2, true);
	v_mfma_f32_32x32x16_bf16 v[48:63], v[108:111], v[80:83], v[48:63]
	v_cvt_pk_bf16_f32 v86, v89, v116
	v_cvt_pk_bf16_f32 v87, v117, v118
	v_mfma_f32_32x32x16_bf16 v[64:79], v[100:103], v[80:83], v[64:79]
	v_add_u32_e32 v80, 0x2000, v198
	v_mfma_f32_32x32x16_bf16 v[48:63], v[104:107], v[84:87], v[48:63]
	v_mfma_f32_32x32x16_bf16 v[64:79], v[96:99], v[84:87], v[64:79]
	ds_read_b128 v[114:117], v198
	ds_read_b128 v[118:121], v198 offset:1024
	ds_read_b128 v[122:125], v198 offset:2048
	ds_read_b128 v[144:147], v198 offset:3072
	ds_read_b128 v[108:111], v80
	ds_read_b128 v[100:103], v80 offset:1024
	ds_read_b128 v[104:107], v80 offset:2048
	ds_read_b128 v[96:99], v80 offset:3072
	s_waitcnt lgkmcnt(4)
	v_add_u32_e32 v80, 0xc0, v113
	v_cvt_f32_i32_e32 v80, v80
	v_mul_f32_e32 v80, v163, v80
	v_add_f32_e64 v94, v176, v80
	v_add_f32_e64 v95, v177, v80
	v_pk_add_f32 v[92:93], v[174:175], v[80:81] op_sel_hi:[1,0]
	v_pk_add_f32 v[90:91], v[172:173], v[80:81] op_sel_hi:[1,0]
	v_pk_add_f32 v[88:89], v[170:171], v[80:81] op_sel_hi:[1,0]
	v_pk_add_f32 v[86:87], v[168:169], v[80:81] op_sel_hi:[1,0]
	v_pk_add_f32 v[84:85], v[166:167], v[80:81] op_sel_hi:[1,0]
	v_pk_add_f32 v[82:83], v[164:165], v[80:81] op_sel_hi:[1,0]
	v_pk_add_f32 v[80:81], v[162:163], v[80:81] op_sel_hi:[1,0]
	s_nop 1
	v_mfma_f32_32x32x16_bf16 v[80:95], v[114:117], v[128:131], v[80:95]
	v_mfma_f32_32x32x16_bf16 v[80:95], v[118:121], v[132:135], v[80:95]
	v_mfma_f32_32x32x16_bf16 v[80:95], v[122:125], v[136:139], v[80:95]
	v_mfma_f32_32x32x16_bf16 v[80:95], v[144:147], v[140:143], v[80:95]
	s_nop 11
	v_cndmask_b32_e64 v120, v80, v190, s[70:71]
	v_cndmask_b32_e64 v119, v81, v190, s[70:71]
	v_cndmask_b32_e64 v118, v82, v190, s[70:71]
	v_cndmask_b32_e64 v117, v83, v190, s[70:71]
	v_cndmask_b32_e64 v116, v84, v190, s[70:71]
	v_cndmask_b32_e64 v115, v85, v190, s[70:71]
	v_cndmask_b32_e64 v114, v86, v190, s[70:71]
	v_cndmask_b32_e64 v113, v87, v190, s[70:71]
	v_cndmask_b32_e64 v87, v88, v190, s[70:71]
	v_cndmask_b32_e64 v86, v89, v190, s[70:71]
	v_cndmask_b32_e64 v85, v90, v190, s[70:71]
	v_cndmask_b32_e64 v84, v91, v190, s[70:71]
	v_cndmask_b32_e64 v83, v92, v190, s[70:71]
	v_cndmask_b32_e64 v82, v93, v190, s[70:71]
	v_cndmask_b32_e64 v81, v94, v190, s[70:71]
	v_cndmask_b32_e64 v80, v95, v190, s[70:71]
	s_nop 11
	v_max3_f32 v90, v120, v119, v118
	v_max3_f32 v88, v117, v116, v115
	v_max3_f32 v89, v114, v113, v87
	v_max3_f32 v90, v90, v88, v89
	v_max3_f32 v88, v86, v85, v84
	v_max3_f32 v89, v83, v82, v81
	v_max3_f32 v88, v88, v89, v80
	v_max_f32 v90, v90, v88
	s_nop 0
	v_mov_b32_e32 v88, v90
	s_nop 1
	v_permlane32_swap_b32_e32 v90, v88
	v_max_f32 v88, v90, v88
	s_nop 0
	v_cmp_gt_f32_e32 vcc, v88, v196
	s_cbranch_vccz .LBB0_1336
	v_max3_f32 v89, v196, v88, s86
	v_sub_f32_e32 v88, v196, v89
	v_exp_f32_e32 v88, v88
	v_mov_b32_e32 v196, v89
	v_mul_f32_e32 v112, v88, v112
	v_pk_mul_f32 v[62:63], v[62:63], v[88:89] op_sel_hi:[1,0]
	v_pk_mul_f32 v[60:61], v[60:61], v[88:89] op_sel_hi:[1,0]
	v_pk_mul_f32 v[58:59], v[58:59], v[88:89] op_sel_hi:[1,0]
	v_pk_mul_f32 v[56:57], v[56:57], v[88:89] op_sel_hi:[1,0]
	v_pk_mul_f32 v[54:55], v[54:55], v[88:89] op_sel_hi:[1,0]
	v_pk_mul_f32 v[52:53], v[52:53], v[88:89] op_sel_hi:[1,0]
	v_pk_mul_f32 v[50:51], v[50:51], v[88:89] op_sel_hi:[1,0]
	v_pk_mul_f32 v[48:49], v[48:49], v[88:89] op_sel_hi:[1,0]
	v_pk_mul_f32 v[78:79], v[78:79], v[88:89] op_sel_hi:[1,0]
	v_pk_mul_f32 v[76:77], v[76:77], v[88:89] op_sel_hi:[1,0]
	v_pk_mul_f32 v[74:75], v[74:75], v[88:89] op_sel_hi:[1,0]
	v_pk_mul_f32 v[72:73], v[72:73], v[88:89] op_sel_hi:[1,0]
	v_pk_mul_f32 v[70:71], v[70:71], v[88:89] op_sel_hi:[1,0]
	v_pk_mul_f32 v[68:69], v[68:69], v[88:89] op_sel_hi:[1,0]
	v_pk_mul_f32 v[66:67], v[66:67], v[88:89] op_sel_hi:[1,0]
	v_pk_mul_f32 v[64:65], v[64:65], v[88:89] op_sel_hi:[1,0]
.LBB0_1336:
	v_sub_f32_e32 v88, v120, v196
	v_sub_f32_e32 v89, v119, v196
	v_sub_f32_e32 v90, v118, v196
	v_sub_f32_e32 v92, v117, v196
	v_sub_f32_e32 v93, v116, v196
	v_sub_f32_e32 v94, v115, v196
	v_sub_f32_e32 v95, v114, v196
	v_sub_f32_e32 v113, v113, v196
	v_exp_f32_e32 v88, v88
	v_exp_f32_e32 v89, v89
	v_exp_f32_e32 v90, v90
	v_exp_f32_e32 v92, v92
	v_exp_f32_e32 v93, v93
	v_exp_f32_e32 v94, v94
	v_exp_f32_e32 v95, v95
	v_exp_f32_e32 v113, v113
	v_sub_f32_e32 v85, v85, v196
	v_sub_f32_e32 v84, v84, v196
	v_sub_f32_e32 v83, v83, v196
	v_sub_f32_e32 v82, v82, v196
	v_add_f32_e32 v91, 0, v88
	v_exp_f32_e32 v116, v85
	v_exp_f32_e32 v117, v84
	v_exp_f32_e32 v118, v83
	v_exp_f32_e32 v119, v82
	v_cvt_pk_bf16_f32 v82, v88, v89
	v_cvt_pk_bf16_f32 v83, v90, v92
	v_cvt_pk_bf16_f32 v84, v93, v94
	v_cvt_pk_bf16_f32 v85, v95, v113
	v_add_f32_e32 v91, v89, v91
	v_add_f32_e32 v91, v90, v91
	s_waitcnt lgkmcnt(0)
	v_mfma_f32_32x32x16_bf16 v[48:63], v[108:111], v[82:85], v[48:63]
	v_sub_f32_e32 v87, v87, v196
	v_sub_f32_e32 v86, v86, v196
	v_sub_f32_e32 v81, v81, v196
	v_sub_f32_e32 v80, v80, v196
	v_add_f32_e32 v90, v92, v91
	v_exp_f32_e32 v114, v87
	v_exp_f32_e32 v115, v86
	v_mfma_f32_32x32x16_bf16 v[64:79], v[100:103], v[82:85], v[64:79]
	v_exp_f32_e32 v81, v81
	v_exp_f32_e32 v80, v80
	v_add_f32_e32 v90, v93, v90
	v_add_f32_e32 v90, v94, v90
	v_add_f32_e32 v90, v95, v90
	v_add_f32_e32 v90, v113, v90
	v_cvt_pk_bf16_f32 v86, v114, v115
	v_cvt_pk_bf16_f32 v87, v116, v117
	v_cvt_pk_bf16_f32 v88, v118, v119
	v_cvt_pk_bf16_f32 v89, v81, v80
	v_add_f32_e32 v90, v114, v90
	v_add_f32_e32 v90, v115, v90
	v_mfma_f32_32x32x16_bf16 v[48:63], v[104:107], v[86:89], v[48:63]
	v_add_f32_e32 v82, v116, v90
	v_add_f32_e32 v82, v117, v82
	v_add_f32_e32 v82, v118, v82
	v_add_f32_e32 v82, v119, v82
	v_add_f32_e32 v81, v81, v82
	v_add_f32_e32 v80, v80, v81
	v_add_f32_e32 v197, v112, v80
	v_mfma_f32_32x32x16_bf16 v[64:79], v[96:99], v[86:89], v[64:79]
.LBB0_1337:
	s_add_i32 s0, s72, 1
	s_sub_i32 s89, s89, 64
	s_and_b32 s72, s0, 3
	s_add_i32 s92, s92, -1
	s_add_i32 s0, s75, s89
	s_cmp_lg_u32 s0, 0
	s_movk_i32 s0, 0xe000
	s_mov_b32 s1, -1
	v_lshl_add_u64 v[180:181], v[180:181], 0, s[0:1]
	s_cbranch_scc0 .Lmoba_ip_exit
	s_cmp_lt_u32 s92, 2
	s_mov_b64 s[0:1], -1
	s_cbranch_scc0 .LBB0_1305
	s_branch .LBB0_1300
.Lmoba_ip_exit:
	s_nop 11
	v_mov_b64_e32 v[94:95], v[78:79]
	v_mov_b64_e32 v[110:111], v[62:63]
	v_mov_b32_e32 v199, v196
	v_mov_b32_e32 v116, v197
	v_mov_b64_e32 v[92:93], v[76:77]
	v_mov_b64_e32 v[90:91], v[74:75]
	v_mov_b64_e32 v[88:89], v[72:73]
	v_mov_b64_e32 v[86:87], v[70:71]
	v_mov_b64_e32 v[84:85], v[68:69]
	v_mov_b64_e32 v[82:83], v[66:67]
	v_mov_b64_e32 v[80:81], v[64:65]
	v_mov_b64_e32 v[108:109], v[60:61]
	v_mov_b64_e32 v[106:107], v[58:59]
	v_mov_b64_e32 v[104:105], v[56:57]
	v_mov_b64_e32 v[102:103], v[54:55]
	v_mov_b64_e32 v[100:101], v[52:53]
	v_mov_b64_e32 v[98:99], v[50:51]
	v_mov_b64_e32 v[96:97], v[48:49]
	s_branch .Lmoba_epi

; __device__ __forceinline__ unsigned pk2(float lo, float hi) { const f32x2_pk v = {lo, hi}; return __builtin_bit_cast(unsigned, __builtin_convertvector(v, bf16x2)); }
; __device__ __forceinline__ void attn_moba_unit(Frame& F, const bf16_t* Qh, const bf16_t* Kh, const bf16_t* Vth, const float* KMh, const float slope2, const int qb, bf16_t* AOp) {
;     ...
;     const float linv = 1.f / (l + __shfl_xor(l, 32));
;     bf16_t* orow = AOp + (size_t)q * DM;
; #pragma unroll
;     for (int g = 0; g < 4; ++g) { u32x2 w;
;         w.x = pk2(O0[4 * g] * linv, O0[4 * g + 1] * linv); w.y = pk2(O0[4 * g + 2] * linv, O0[4 * g + 3] * linv); *(u32x2*)(orow + 8 * g + 4 * hi) = w;
;         w.x = pk2(O1[4 * g] * linv, O1[4 * g + 1] * linv); w.y = pk2(O1[4 * g + 2] * linv, O1[4 * g + 3] * linv); *(u32x2*)(orow + 32 + 8 * g + 4 * hi) = w; }
;     asm volatile("s_waitcnt vmcnt(0) lgkmcnt(0)" ::: "memory"); __builtin_amdgcn_s_barrier();
.Lmoba_epi:
	ds_bpermute_b32 v0, v192, v116
	s_add_i32 s94, s94, 1
	s_cmp_eq_u32 s94, 4
	s_mov_b32 s14, 0xff800000
	s_waitcnt lgkmcnt(0)
	v_add_f32_e32 v0, v116, v0
	v_div_scale_f32 v1, s[0:1], v0, v0, 1.0
	v_rcp_f32_e32 v2, v1
	s_nop 0
	v_fma_f32 v3, -v1, v2, 1.0
	v_fmac_f32_e32 v2, v3, v2
	v_div_scale_f32 v3, vcc, 1.0, v0, 1.0
	v_mul_f32_e32 v4, v3, v2
	v_fma_f32 v5, -v1, v4, v3
	v_fmac_f32_e32 v4, v5, v2
	v_fma_f32 v1, -v1, v4, v3
	v_div_fmas_f32 v1, v1, v2, v4
	v_lshlrev_b64 v[2:3], 11, v[160:161]
	v_lshlrev_b32_e32 v4, 2, v191
	v_div_fixup_f32 v0, v1, v0, 1.0
	v_lshl_add_u64 v[2:3], s[76:77], 0, v[2:3]
	v_ashrrev_i32_e32 v5, 31, v4
	v_lshl_add_u64 v[2:3], v[4:5], 1, v[2:3]
	v_pk_mul_f32 v[4:5], v[96:97], v[0:1] op_sel_hi:[1,0]
	v_pk_mul_f32 v[6:7], v[98:99], v[0:1] op_sel_hi:[1,0]
	v_cvt_pk_bf16_f32 v4, v4, v5
	v_cvt_pk_bf16_f32 v5, v6, v7
	global_store_dwordx2 v[2:3], v[4:5], off offset:1024
	v_pk_mul_f32 v[4:5], v[80:81], v[0:1] op_sel_hi:[1,0]
	v_pk_mul_f32 v[6:7], v[82:83], v[0:1] op_sel_hi:[1,0]
	v_cvt_pk_bf16_f32 v4, v4, v5
	v_cvt_pk_bf16_f32 v5, v6, v7
	global_store_dwordx2 v[2:3], v[4:5], off offset:1088
	v_pk_mul_f32 v[4:5], v[100:101], v[0:1] op_sel_hi:[1,0]
	v_pk_mul_f32 v[6:7], v[102:103], v[0:1] op_sel_hi:[1,0]
	v_cvt_pk_bf16_f32 v4, v4, v5
	v_cvt_pk_bf16_f32 v5, v6, v7
	global_store_dwordx2 v[2:3], v[4:5], off offset:1040
	v_pk_mul_f32 v[4:5], v[84:85], v[0:1] op_sel_hi:[1,0]
	v_pk_mul_f32 v[6:7], v[86:87], v[0:1] op_sel_hi:[1,0]
	v_cvt_pk_bf16_f32 v4, v4, v5
	v_cvt_pk_bf16_f32 v5, v6, v7
	global_store_dwordx2 v[2:3], v[4:5], off offset:1104
	v_pk_mul_f32 v[4:5], v[104:105], v[0:1] op_sel_hi:[1,0]
	v_pk_mul_f32 v[6:7], v[106:107], v[0:1] op_sel_hi:[1,0]
	v_cvt_pk_bf16_f32 v4, v4, v5
	v_cvt_pk_bf16_f32 v5, v6, v7
	global_store_dwordx2 v[2:3], v[4:5], off offset:1056
	v_pk_mul_f32 v[4:5], v[88:89], v[0:1] op_sel_hi:[1,0]
	v_pk_mul_f32 v[6:7], v[90:91], v[0:1] op_sel_hi:[1,0]
	v_cvt_pk_bf16_f32 v4, v4, v5
	v_cvt_pk_bf16_f32 v5, v6, v7
	global_store_dwordx2 v[2:3], v[4:5], off offset:1120
	v_pk_mul_f32 v[4:5], v[108:109], v[0:1] op_sel_hi:[1,0]
	v_pk_mul_f32 v[6:7], v[110:111], v[0:1] op_sel_hi:[1,0]
	v_cvt_pk_bf16_f32 v4, v4, v5
	v_cvt_pk_bf16_f32 v5, v6, v7
	global_store_dwordx2 v[2:3], v[4:5], off offset:1072
	v_pk_mul_f32 v[4:5], v[92:93], v[0:1] op_sel_hi:[1,0]
	v_pk_mul_f32 v[0:1], v[94:95], v[0:1] op_sel_hi:[1,0]
	v_cvt_pk_bf16_f32 v4, v4, v5
	v_cvt_pk_bf16_f32 v5, v0, v1
	global_store_dwordx2 v[2:3], v[4:5], off offset:1136
	s_waitcnt vmcnt(0) lgkmcnt(0)
	s_barrier
	s_cbranch_scc0 .LBB0_1285
	s_branch .LBB0_1277
